# snake MFMA order + de-serialised rs cache fill + load segments slimmed (one s_waitcnt instead of two, no s_nop where an address add separates the m0 write from the LDS-DMA)
# speedup vs baseline: 1.0030x; 1.0018x over previous
.LBB0_130:
	ds_read_b128 v[144:147], v140
	ds_read_b128 v[148:151], v140 offset:1024
	ds_read_b128 v[152:155], v140 offset:2048
	ds_read_b128 v[156:159], v140 offset:3072
	ds_read_b128 v[164:167], v141
	ds_read_b128 v[168:171], v141 offset:1024
	ds_read_b128 v[172:175], v141 offset:2048
	ds_read_b128 v[176:179], v141 offset:3072
	s_add_u32 s31, s10, 0xfff7c080
	s_addc_u32 s53, s11, -1
	s_cmp_eq_u32 s30, 28
	s_cselect_b32 s55, s25, s53
	s_cselect_b32 s54, s24, s31
	s_cselect_b32 s57, s4, s29
	s_cselect_b32 s56, s5, s28
	s_mov_b32 m0, s23
	ds_read_b128 v[180:183], v163
	ds_read_b128 v[190:193], v163 offset:1024
	ds_read_b128 v[194:197], v163 offset:2048
	ds_read_b128 v[198:201], v163 offset:3072
	ds_read_b128 v[202:205], v163 offset:4096
	ds_read_b128 v[206:209], v163 offset:5120
	ds_read_b128 v[216:219], v163 offset:6144
	ds_read_b128 v[220:223], v163 offset:7168
	global_load_lds_dwordx4 v138, s[10:11]
	s_mov_b32 m0, s33
	s_add_u32 s70, s10, s96
	s_addc_u32 s71, s11, s97
	global_load_lds_dwordx4 v138, s[70:71]
	s_waitcnt vmcnt(8) lgkmcnt(0)
	s_barrier
	v_mfma_f32_16x16x32_bf16 v[120:123], v[144:147], v[180:183], v[120:123]
	v_mfma_f32_16x16x32_bf16 v[120:123], v[148:151], v[190:193], v[120:123]
	v_mfma_f32_16x16x32_bf16 v[116:119], v[152:155], v[180:183], v[116:119]
	v_mfma_f32_16x16x32_bf16 v[116:119], v[156:159], v[190:193], v[116:119]
	v_mfma_f32_16x16x32_bf16 v[128:131], v[164:167], v[180:183], v[128:131]
	v_mfma_f32_16x16x32_bf16 v[128:131], v[168:171], v[190:193], v[128:131]
	v_mfma_f32_16x16x32_bf16 v[124:127], v[172:175], v[180:183], v[124:127]
	v_mfma_f32_16x16x32_bf16 v[124:127], v[176:179], v[190:193], v[124:127]
	v_mfma_f32_16x16x32_bf16 v[108:111], v[172:175], v[194:197], v[108:111]
	v_mfma_f32_16x16x32_bf16 v[108:111], v[176:179], v[198:201], v[108:111]
	v_mfma_f32_16x16x32_bf16 v[112:115], v[164:167], v[194:197], v[112:115]
	v_mfma_f32_16x16x32_bf16 v[112:115], v[168:171], v[198:201], v[112:115]
	v_mfma_f32_16x16x32_bf16 v[100:103], v[152:155], v[194:197], v[100:103]
	v_mfma_f32_16x16x32_bf16 v[100:103], v[156:159], v[198:201], v[100:103]
	v_mfma_f32_16x16x32_bf16 v[104:107], v[144:147], v[194:197], v[104:107]
	v_mfma_f32_16x16x32_bf16 v[104:107], v[148:151], v[198:201], v[104:107]
	v_mfma_f32_16x16x32_bf16 v[88:91], v[144:147], v[202:205], v[88:91]
	v_mfma_f32_16x16x32_bf16 v[88:91], v[148:151], v[206:209], v[88:91]
	v_mfma_f32_16x16x32_bf16 v[84:87], v[152:155], v[202:205], v[84:87]
	v_mfma_f32_16x16x32_bf16 v[84:87], v[156:159], v[206:209], v[84:87]
	v_mfma_f32_16x16x32_bf16 v[96:99], v[164:167], v[202:205], v[96:99]
	v_mfma_f32_16x16x32_bf16 v[96:99], v[168:171], v[206:209], v[96:99]
	v_mfma_f32_16x16x32_bf16 v[92:95], v[172:175], v[202:205], v[92:95]
	v_mfma_f32_16x16x32_bf16 v[92:95], v[176:179], v[206:209], v[92:95]
	v_mfma_f32_16x16x32_bf16 v[76:79], v[172:175], v[216:219], v[76:79]
	v_mfma_f32_16x16x32_bf16 v[76:79], v[176:179], v[220:223], v[76:79]
	v_mfma_f32_16x16x32_bf16 v[80:83], v[164:167], v[216:219], v[80:83]
	v_mfma_f32_16x16x32_bf16 v[80:83], v[168:171], v[220:223], v[80:83]
	v_mfma_f32_16x16x32_bf16 v[68:71], v[152:155], v[216:219], v[68:71]
	v_mfma_f32_16x16x32_bf16 v[68:71], v[156:159], v[220:223], v[68:71]
	v_mfma_f32_16x16x32_bf16 v[72:75], v[144:147], v[216:219], v[72:75]
	v_mfma_f32_16x16x32_bf16 v[72:75], v[148:151], v[220:223], v[72:75]
	s_barrier
	s_mov_b32 m0, s45
	ds_read_b128 v[180:183], v163 offset:16384
	ds_read_b128 v[190:193], v163 offset:17408
	ds_read_b128 v[194:197], v163 offset:18432
	ds_read_b128 v[198:201], v163 offset:19456
	ds_read_b128 v[202:205], v163 offset:20480
	ds_read_b128 v[206:209], v163 offset:21504
	ds_read_b128 v[216:219], v163 offset:22528
	ds_read_b128 v[220:223], v163 offset:23552
	global_load_lds_dwordx4 v132, s[56:57]
	s_mov_b32 m0, s46
	s_add_u32 s70, s56, s90
	s_addc_u32 s71, s57, s91
	global_load_lds_dwordx4 v132, s[70:71]
	s_mov_b32 m0, s47
	s_add_u32 s70, s56, s60
	s_addc_u32 s71, s57, s61
	global_load_lds_dwordx4 v132, s[70:71]
	s_mov_b32 m0, s48
	s_add_u32 s70, s56, s64
	s_addc_u32 s71, s57, s65
	global_load_lds_dwordx4 v132, s[70:71]
	s_mov_b32 m0, s37
	s_nop 0
	global_load_lds_dwordx4 v134, s[54:55]
	s_mov_b32 m0, s38
	s_add_u32 s70, s54, s96
	s_addc_u32 s71, s55, s97
	global_load_lds_dwordx4 v134, s[70:71]
	s_waitcnt vmcnt(8) lgkmcnt(0)
	s_barrier
	v_mfma_f32_16x16x32_bf16 v[56:59], v[144:147], v[180:183], v[56:59]
	v_mfma_f32_16x16x32_bf16 v[56:59], v[148:151], v[190:193], v[56:59]
	v_mfma_f32_16x16x32_bf16 v[52:55], v[152:155], v[180:183], v[52:55]
	v_mfma_f32_16x16x32_bf16 v[52:55], v[156:159], v[190:193], v[52:55]
	v_mfma_f32_16x16x32_bf16 v[64:67], v[164:167], v[180:183], v[64:67]
	v_mfma_f32_16x16x32_bf16 v[64:67], v[168:171], v[190:193], v[64:67]
	v_mfma_f32_16x16x32_bf16 v[60:63], v[172:175], v[180:183], v[60:63]
	v_mfma_f32_16x16x32_bf16 v[60:63], v[176:179], v[190:193], v[60:63]
	v_mfma_f32_16x16x32_bf16 v[44:47], v[172:175], v[194:197], v[44:47]
	v_mfma_f32_16x16x32_bf16 v[44:47], v[176:179], v[198:201], v[44:47]
	v_mfma_f32_16x16x32_bf16 v[48:51], v[164:167], v[194:197], v[48:51]
	v_mfma_f32_16x16x32_bf16 v[48:51], v[168:171], v[198:201], v[48:51]
	v_mfma_f32_16x16x32_bf16 v[36:39], v[152:155], v[194:197], v[36:39]
	v_mfma_f32_16x16x32_bf16 v[36:39], v[156:159], v[198:201], v[36:39]
	v_mfma_f32_16x16x32_bf16 v[40:43], v[144:147], v[194:197], v[40:43]
	v_mfma_f32_16x16x32_bf16 v[40:43], v[148:151], v[198:201], v[40:43]
	v_mfma_f32_16x16x32_bf16 v[24:27], v[144:147], v[202:205], v[24:27]
	v_mfma_f32_16x16x32_bf16 v[24:27], v[148:151], v[206:209], v[24:27]
	v_mfma_f32_16x16x32_bf16 v[20:23], v[152:155], v[202:205], v[20:23]
	v_mfma_f32_16x16x32_bf16 v[20:23], v[156:159], v[206:209], v[20:23]
	v_mfma_f32_16x16x32_bf16 v[32:35], v[164:167], v[202:205], v[32:35]
	v_mfma_f32_16x16x32_bf16 v[32:35], v[168:171], v[206:209], v[32:35]
	v_mfma_f32_16x16x32_bf16 v[28:31], v[172:175], v[202:205], v[28:31]
	v_mfma_f32_16x16x32_bf16 v[28:31], v[176:179], v[206:209], v[28:31]
	v_mfma_f32_16x16x32_bf16 v[12:15], v[172:175], v[216:219], v[12:15]
	v_mfma_f32_16x16x32_bf16 v[12:15], v[176:179], v[220:223], v[12:15]
	v_mfma_f32_16x16x32_bf16 v[16:19], v[164:167], v[216:219], v[16:19]
	v_mfma_f32_16x16x32_bf16 v[16:19], v[168:171], v[220:223], v[16:19]
	v_mfma_f32_16x16x32_bf16 v[4:7], v[152:155], v[216:219], v[4:7]
	v_mfma_f32_16x16x32_bf16 v[4:7], v[156:159], v[220:223], v[4:7]
	v_mfma_f32_16x16x32_bf16 v[8:11], v[144:147], v[216:219], v[8:11]
	v_mfma_f32_16x16x32_bf16 v[8:11], v[148:151], v[220:223], v[8:11]
	s_barrier
; #define PG8_MMA(ai, bj, At, Bt) do { __builtin_amdgcn_s_setprio(1); _Pragma("unroll") for (int m = 0; m < 4; ++m) _Pragma("unroll") for (int n = 0; n < 2; ++n) _Pragma("unroll") for (int k = 0; k < 2; ++k) \
;         acc[ai][bj][m][n] = __builtin_amdgcn_mfma_f32_16x16x32_bf16(Bt[n][k], At[m][k], acc[ai][bj][m][n], 0, 0, 0); __builtin_amdgcn_s_setprio(0); } while (0)
; #define PG8_WAIT_V(n) asm volatile("s_waitcnt vmcnt(" #n ")" ::: "memory")
; #define PG8_TRIP_HEAD(T) const int t = (T); const bool last = (t == nt - 2); \
;             const char* a1 = cA + (size_t)(t + 1) * kstep; \
;             const char* a2 = last ? nA : cA + (size_t)(t + 2) * kstep; const char* b2 = last ? nB : cB + (size_t)(t + 2) * kstep; \
;             const char* a3 = a2 + kstep; const char* b3 = b2 + kstep; \
;             if (last && has_next) S.a_ready(nxt);
; template <class Epi, class Sched, bool ALIGN_EPI = false, bool SP2 = false>
; __device__ __forceinline__ void gemm_phase(PG8_LAS unsigned char* lds, const Gemm g, const Sched& S, const Epi& E) {
;     ...
;         if constexpr (SP2) {
;             { PG8_TRIP_HEAD(0) PG8_TRIP_SP2(asm volatile("s_waitcnt vmcnt(%0)" :: "n"(8 + Epi::NST) : "memory"), PG8_MMAZ) }
;             for (int tt = 2; tt < nt; tt += 2) { PG8_TRIP_HEAD(tt) PG8_TRIP_SP2(PG8_WAIT_V(8), PG8_MMA) }
	ds_read_b128 v[144:147], v142
	ds_read_b128 v[148:151], v142 offset:1024
	ds_read_b128 v[152:155], v142 offset:2048
	ds_read_b128 v[156:159], v142 offset:3072
	ds_read_b128 v[164:167], v143
	ds_read_b128 v[168:171], v143 offset:1024
	ds_read_b128 v[172:175], v143 offset:2048
	ds_read_b128 v[176:179], v143 offset:3072
	s_mov_b32 m0, s39
	ds_read_b128 v[180:183], v163 offset:32768
	ds_read_b128 v[190:193], v163 offset:33792
	ds_read_b128 v[194:197], v163 offset:34816
	ds_read_b128 v[198:201], v163 offset:35840
	ds_read_b128 v[202:205], v163 offset:36864
	ds_read_b128 v[206:209], v163 offset:37888
	ds_read_b128 v[216:219], v163 offset:38912
	ds_read_b128 v[220:223], v163 offset:39936
	s_add_u32 s70, s54, s82
	s_addc_u32 s71, s55, s83
	global_load_lds_dwordx4 v134, s[70:71]
	s_mov_b32 m0, s40
	s_add_u32 s70, s54, s68
	s_addc_u32 s71, s55, s69
	global_load_lds_dwordx4 v134, s[70:71]
	s_waitcnt vmcnt(8) lgkmcnt(0)
	s_barrier
	v_mfma_f32_16x16x32_bf16 v[120:123], v[144:147], v[180:183], v[120:123]
	v_mfma_f32_16x16x32_bf16 v[120:123], v[148:151], v[190:193], v[120:123]
	v_mfma_f32_16x16x32_bf16 v[116:119], v[152:155], v[180:183], v[116:119]
	v_mfma_f32_16x16x32_bf16 v[116:119], v[156:159], v[190:193], v[116:119]
	v_mfma_f32_16x16x32_bf16 v[128:131], v[164:167], v[180:183], v[128:131]
	v_mfma_f32_16x16x32_bf16 v[128:131], v[168:171], v[190:193], v[128:131]
	v_mfma_f32_16x16x32_bf16 v[124:127], v[172:175], v[180:183], v[124:127]
	v_mfma_f32_16x16x32_bf16 v[124:127], v[176:179], v[190:193], v[124:127]
	v_mfma_f32_16x16x32_bf16 v[108:111], v[172:175], v[194:197], v[108:111]
	v_mfma_f32_16x16x32_bf16 v[108:111], v[176:179], v[198:201], v[108:111]
	v_mfma_f32_16x16x32_bf16 v[112:115], v[164:167], v[194:197], v[112:115]
	v_mfma_f32_16x16x32_bf16 v[112:115], v[168:171], v[198:201], v[112:115]
	v_mfma_f32_16x16x32_bf16 v[100:103], v[152:155], v[194:197], v[100:103]
	v_mfma_f32_16x16x32_bf16 v[100:103], v[156:159], v[198:201], v[100:103]
	v_mfma_f32_16x16x32_bf16 v[104:107], v[144:147], v[194:197], v[104:107]
	v_mfma_f32_16x16x32_bf16 v[104:107], v[148:151], v[198:201], v[104:107]
	v_mfma_f32_16x16x32_bf16 v[88:91], v[144:147], v[202:205], v[88:91]
	v_mfma_f32_16x16x32_bf16 v[88:91], v[148:151], v[206:209], v[88:91]
	v_mfma_f32_16x16x32_bf16 v[84:87], v[152:155], v[202:205], v[84:87]
	v_mfma_f32_16x16x32_bf16 v[84:87], v[156:159], v[206:209], v[84:87]
	v_mfma_f32_16x16x32_bf16 v[96:99], v[164:167], v[202:205], v[96:99]
	v_mfma_f32_16x16x32_bf16 v[96:99], v[168:171], v[206:209], v[96:99]
	v_mfma_f32_16x16x32_bf16 v[92:95], v[172:175], v[202:205], v[92:95]
	v_mfma_f32_16x16x32_bf16 v[92:95], v[176:179], v[206:209], v[92:95]
	v_mfma_f32_16x16x32_bf16 v[76:79], v[172:175], v[216:219], v[76:79]
	v_mfma_f32_16x16x32_bf16 v[76:79], v[176:179], v[220:223], v[76:79]
	v_mfma_f32_16x16x32_bf16 v[80:83], v[164:167], v[216:219], v[80:83]
	v_mfma_f32_16x16x32_bf16 v[80:83], v[168:171], v[220:223], v[80:83]
	v_mfma_f32_16x16x32_bf16 v[68:71], v[152:155], v[216:219], v[68:71]
	v_mfma_f32_16x16x32_bf16 v[68:71], v[156:159], v[220:223], v[68:71]
	v_mfma_f32_16x16x32_bf16 v[72:75], v[144:147], v[216:219], v[72:75]
	v_mfma_f32_16x16x32_bf16 v[72:75], v[148:151], v[220:223], v[72:75]
	s_barrier
	s_mov_b32 m0, s49
	ds_read_b128 v[180:183], v163 offset:49152
	ds_read_b128 v[190:193], v163 offset:50176
	ds_read_b128 v[194:197], v163 offset:51200
	ds_read_b128 v[198:201], v163 offset:52224
	ds_read_b128 v[202:205], v163 offset:53248
	ds_read_b128 v[206:209], v163 offset:54272
	ds_read_b128 v[216:219], v163 offset:55296
	ds_read_b128 v[220:223], v163 offset:56320
	s_add_u32 s70, s56, s78
	s_addc_u32 s71, s57, s79
	global_load_lds_dwordx4 v132, s[70:71]
	s_mov_b32 m0, s50
	s_add_u32 s70, s56, s84
	s_addc_u32 s71, s57, s85
	global_load_lds_dwordx4 v132, s[70:71]
	s_mov_b32 m0, s51
	s_add_u32 s70, s56, s62
	s_addc_u32 s71, s57, s63
	global_load_lds_dwordx4 v132, s[70:71]
	s_mov_b32 m0, s52
	s_add_u32 s70, s56, s66
	s_addc_u32 s71, s57, s67
	global_load_lds_dwordx4 v132, s[70:71]
	s_mov_b32 m0, s0
	s_add_u32 s70, s54, s78
	s_addc_u32 s71, s55, s79
	global_load_lds_dwordx4 v134, s[70:71]
	s_mov_b32 m0, s41
	s_add_u32 s70, s54, s92
	s_addc_u32 s71, s55, s93
	global_load_lds_dwordx4 v134, s[70:71]
	s_waitcnt vmcnt(8) lgkmcnt(0)
	s_barrier
	v_mfma_f32_16x16x32_bf16 v[56:59], v[144:147], v[180:183], v[56:59]
	v_mfma_f32_16x16x32_bf16 v[56:59], v[148:151], v[190:193], v[56:59]
	v_mfma_f32_16x16x32_bf16 v[52:55], v[152:155], v[180:183], v[52:55]
	v_mfma_f32_16x16x32_bf16 v[52:55], v[156:159], v[190:193], v[52:55]
	v_mfma_f32_16x16x32_bf16 v[64:67], v[164:167], v[180:183], v[64:67]
	v_mfma_f32_16x16x32_bf16 v[64:67], v[168:171], v[190:193], v[64:67]
	v_mfma_f32_16x16x32_bf16 v[60:63], v[172:175], v[180:183], v[60:63]
	v_mfma_f32_16x16x32_bf16 v[60:63], v[176:179], v[190:193], v[60:63]
	v_mfma_f32_16x16x32_bf16 v[44:47], v[172:175], v[194:197], v[44:47]
	v_mfma_f32_16x16x32_bf16 v[44:47], v[176:179], v[198:201], v[44:47]
	v_mfma_f32_16x16x32_bf16 v[48:51], v[164:167], v[194:197], v[48:51]
	v_mfma_f32_16x16x32_bf16 v[48:51], v[168:171], v[198:201], v[48:51]
	v_mfma_f32_16x16x32_bf16 v[36:39], v[152:155], v[194:197], v[36:39]
	v_mfma_f32_16x16x32_bf16 v[36:39], v[156:159], v[198:201], v[36:39]
	v_mfma_f32_16x16x32_bf16 v[40:43], v[144:147], v[194:197], v[40:43]
	v_mfma_f32_16x16x32_bf16 v[40:43], v[148:151], v[198:201], v[40:43]
	v_mfma_f32_16x16x32_bf16 v[24:27], v[144:147], v[202:205], v[24:27]
	v_mfma_f32_16x16x32_bf16 v[24:27], v[148:151], v[206:209], v[24:27]
	v_mfma_f32_16x16x32_bf16 v[20:23], v[152:155], v[202:205], v[20:23]
	v_mfma_f32_16x16x32_bf16 v[20:23], v[156:159], v[206:209], v[20:23]
	v_mfma_f32_16x16x32_bf16 v[32:35], v[164:167], v[202:205], v[32:35]
	v_mfma_f32_16x16x32_bf16 v[32:35], v[168:171], v[206:209], v[32:35]
	v_mfma_f32_16x16x32_bf16 v[28:31], v[172:175], v[202:205], v[28:31]
	v_mfma_f32_16x16x32_bf16 v[28:31], v[176:179], v[206:209], v[28:31]
	v_mfma_f32_16x16x32_bf16 v[12:15], v[172:175], v[216:219], v[12:15]
	v_mfma_f32_16x16x32_bf16 v[12:15], v[176:179], v[220:223], v[12:15]
	v_mfma_f32_16x16x32_bf16 v[16:19], v[164:167], v[216:219], v[16:19]
	v_mfma_f32_16x16x32_bf16 v[16:19], v[168:171], v[220:223], v[16:19]
	v_mfma_f32_16x16x32_bf16 v[4:7], v[152:155], v[216:219], v[4:7]
	v_mfma_f32_16x16x32_bf16 v[4:7], v[156:159], v[220:223], v[4:7]
	v_mfma_f32_16x16x32_bf16 v[8:11], v[144:147], v[216:219], v[8:11]
	v_mfma_f32_16x16x32_bf16 v[8:11], v[148:151], v[220:223], v[8:11]
	s_barrier
	s_add_i32 s30, s30, 2
	s_add_u32 s10, s10, 0x100
	s_addc_u32 s11, s11, 0
	s_add_u32 s28, s28, 0x100
	s_addc_u32 s29, s29, 0
	s_cmp_gt_u32 s30, 29
	s_cbranch_scc0 .LBB0_130
	s_and_b64 vcc, exec, s[20:21]
	s_cbranch_vccz .LBB0_133
	s_barrier

.LBB0_233:
	ds_read_b128 v[120:123], v116
	ds_read_b128 v[132:135], v116 offset:1024
	ds_read_b128 v[144:147], v116 offset:2048
	ds_read_b128 v[148:151], v116 offset:3072
	ds_read_b128 v[152:155], v117
	ds_read_b128 v[156:159], v117 offset:1024
	ds_read_b128 v[166:169], v117 offset:2048
	ds_read_b128 v[170:173], v117 offset:3072
	s_add_u32 s49, s26, 0xffea0080
	s_addc_u32 s50, s27, -1
	s_cmpk_eq_i32 s48, 0x54
	s_cselect_b32 s51, s21, s50
	s_cselect_b32 s50, s20, s49
	s_cselect_b32 s53, s23, s25
	s_cselect_b32 s52, s22, s24
	s_mov_b32 m0, s0
	ds_read_b128 v[180:183], v178
	ds_read_b128 v[184:187], v178 offset:1024
	ds_read_b128 v[190:193], v178 offset:2048
	ds_read_b128 v[194:197], v178 offset:3072
	ds_read_b128 v[198:201], v178 offset:4096
	ds_read_b128 v[202:205], v178 offset:5120
	ds_read_b128 v[206:209], v178 offset:6144
	ds_read_b128 v[216:219], v178 offset:7168
	global_load_lds_dwordx4 v164, s[26:27]
	s_mov_b32 m0, s4
	s_add_u32 s70, s26, s86
	s_addc_u32 s71, s27, s87
	global_load_lds_dwordx4 v164, s[70:71]
	s_waitcnt vmcnt(8) lgkmcnt(0)
	s_barrier
	v_mfma_f32_16x16x32_bf16 v[140:143], v[120:123], v[180:183], v[140:143]
	v_mfma_f32_16x16x32_bf16 v[140:143], v[132:135], v[184:187], v[140:143]
	v_mfma_f32_16x16x32_bf16 v[136:139], v[144:147], v[180:183], v[136:139]
	v_mfma_f32_16x16x32_bf16 v[136:139], v[148:151], v[184:187], v[136:139]
	v_mfma_f32_16x16x32_bf16 v[128:131], v[152:155], v[180:183], v[128:131]
	v_mfma_f32_16x16x32_bf16 v[128:131], v[156:159], v[184:187], v[128:131]
	v_mfma_f32_16x16x32_bf16 v[124:127], v[166:169], v[180:183], v[124:127]
	v_mfma_f32_16x16x32_bf16 v[124:127], v[170:173], v[184:187], v[124:127]
	v_mfma_f32_16x16x32_bf16 v[100:103], v[166:169], v[190:193], v[100:103]
	v_mfma_f32_16x16x32_bf16 v[100:103], v[170:173], v[194:197], v[100:103]
	v_mfma_f32_16x16x32_bf16 v[104:107], v[152:155], v[190:193], v[104:107]
	v_mfma_f32_16x16x32_bf16 v[104:107], v[156:159], v[194:197], v[104:107]
	v_mfma_f32_16x16x32_bf16 v[108:111], v[144:147], v[190:193], v[108:111]
	v_mfma_f32_16x16x32_bf16 v[108:111], v[148:151], v[194:197], v[108:111]
	v_mfma_f32_16x16x32_bf16 v[112:115], v[120:123], v[190:193], v[112:115]
	v_mfma_f32_16x16x32_bf16 v[112:115], v[132:135], v[194:197], v[112:115]
	v_mfma_f32_16x16x32_bf16 v[96:99], v[120:123], v[198:201], v[96:99]
	v_mfma_f32_16x16x32_bf16 v[96:99], v[132:135], v[202:205], v[96:99]
	v_mfma_f32_16x16x32_bf16 v[92:95], v[144:147], v[198:201], v[92:95]
	v_mfma_f32_16x16x32_bf16 v[92:95], v[148:151], v[202:205], v[92:95]
	v_mfma_f32_16x16x32_bf16 v[88:91], v[152:155], v[198:201], v[88:91]
	v_mfma_f32_16x16x32_bf16 v[88:91], v[156:159], v[202:205], v[88:91]
	v_mfma_f32_16x16x32_bf16 v[84:87], v[166:169], v[198:201], v[84:87]
	v_mfma_f32_16x16x32_bf16 v[84:87], v[170:173], v[202:205], v[84:87]
	v_mfma_f32_16x16x32_bf16 v[68:71], v[166:169], v[206:209], v[68:71]
	v_mfma_f32_16x16x32_bf16 v[68:71], v[170:173], v[216:219], v[68:71]
	v_mfma_f32_16x16x32_bf16 v[72:75], v[152:155], v[206:209], v[72:75]
	v_mfma_f32_16x16x32_bf16 v[72:75], v[156:159], v[216:219], v[72:75]
	v_mfma_f32_16x16x32_bf16 v[76:79], v[144:147], v[206:209], v[76:79]
	v_mfma_f32_16x16x32_bf16 v[76:79], v[148:151], v[216:219], v[76:79]
	v_mfma_f32_16x16x32_bf16 v[80:83], v[120:123], v[206:209], v[80:83]
	v_mfma_f32_16x16x32_bf16 v[80:83], v[132:135], v[216:219], v[80:83]
	s_barrier
	s_mov_b32 m0, s5
	ds_read_b128 v[180:183], v178 offset:16384
	ds_read_b128 v[184:187], v178 offset:17408
	ds_read_b128 v[190:193], v178 offset:18432
	ds_read_b128 v[194:197], v178 offset:19456
	ds_read_b128 v[198:201], v178 offset:20480
	ds_read_b128 v[202:205], v178 offset:21504
	ds_read_b128 v[206:209], v178 offset:22528
	ds_read_b128 v[216:219], v178 offset:23552
	global_load_lds_dwordx4 v162, s[52:53]
	s_mov_b32 m0, s33
	s_add_u32 s70, s52, s86
	s_addc_u32 s71, s53, s87
	global_load_lds_dwordx4 v162, s[70:71]
	s_mov_b32 m0, s42
	s_add_u32 s70, s52, s54
	s_addc_u32 s71, s53, s55
	global_load_lds_dwordx4 v162, s[70:71]
	s_mov_b32 m0, s43
	s_add_u32 s70, s52, s56
	s_addc_u32 s71, s53, s57
	global_load_lds_dwordx4 v162, s[70:71]
	s_mov_b32 m0, s31
	s_nop 0
	global_load_lds_dwordx4 v160, s[50:51]
	s_mov_b32 m0, s34
	s_add_u32 s70, s50, s86
	s_addc_u32 s71, s51, s87
	global_load_lds_dwordx4 v160, s[70:71]
	s_waitcnt vmcnt(8) lgkmcnt(0)
	s_barrier
	v_mfma_f32_16x16x32_bf16 v[56:59], v[120:123], v[180:183], v[56:59]
	v_mfma_f32_16x16x32_bf16 v[56:59], v[132:135], v[184:187], v[56:59]
	v_mfma_f32_16x16x32_bf16 v[52:55], v[144:147], v[180:183], v[52:55]
	v_mfma_f32_16x16x32_bf16 v[52:55], v[148:151], v[184:187], v[52:55]
	v_mfma_f32_16x16x32_bf16 v[64:67], v[152:155], v[180:183], v[64:67]
	v_mfma_f32_16x16x32_bf16 v[64:67], v[156:159], v[184:187], v[64:67]
	v_mfma_f32_16x16x32_bf16 v[60:63], v[166:169], v[180:183], v[60:63]
	v_mfma_f32_16x16x32_bf16 v[60:63], v[170:173], v[184:187], v[60:63]
	v_mfma_f32_16x16x32_bf16 v[36:39], v[166:169], v[190:193], v[36:39]
	v_mfma_f32_16x16x32_bf16 v[36:39], v[170:173], v[194:197], v[36:39]
	v_mfma_f32_16x16x32_bf16 v[40:43], v[152:155], v[190:193], v[40:43]
	v_mfma_f32_16x16x32_bf16 v[40:43], v[156:159], v[194:197], v[40:43]
	v_mfma_f32_16x16x32_bf16 v[44:47], v[144:147], v[190:193], v[44:47]
	v_mfma_f32_16x16x32_bf16 v[44:47], v[148:151], v[194:197], v[44:47]
	v_mfma_f32_16x16x32_bf16 v[48:51], v[120:123], v[190:193], v[48:51]
	v_mfma_f32_16x16x32_bf16 v[48:51], v[132:135], v[194:197], v[48:51]
	v_mfma_f32_16x16x32_bf16 v[32:35], v[120:123], v[198:201], v[32:35]
	v_mfma_f32_16x16x32_bf16 v[32:35], v[132:135], v[202:205], v[32:35]
	v_mfma_f32_16x16x32_bf16 v[28:31], v[144:147], v[198:201], v[28:31]
	v_mfma_f32_16x16x32_bf16 v[28:31], v[148:151], v[202:205], v[28:31]
	v_mfma_f32_16x16x32_bf16 v[24:27], v[152:155], v[198:201], v[24:27]
	v_mfma_f32_16x16x32_bf16 v[24:27], v[156:159], v[202:205], v[24:27]
	v_mfma_f32_16x16x32_bf16 v[20:23], v[166:169], v[198:201], v[20:23]
	v_mfma_f32_16x16x32_bf16 v[20:23], v[170:173], v[202:205], v[20:23]
	v_mfma_f32_16x16x32_bf16 v[4:7], v[166:169], v[206:209], v[4:7]
	v_mfma_f32_16x16x32_bf16 v[4:7], v[170:173], v[216:219], v[4:7]
	v_mfma_f32_16x16x32_bf16 v[8:11], v[152:155], v[206:209], v[8:11]
	v_mfma_f32_16x16x32_bf16 v[8:11], v[156:159], v[216:219], v[8:11]
	v_mfma_f32_16x16x32_bf16 v[12:15], v[144:147], v[206:209], v[12:15]
	v_mfma_f32_16x16x32_bf16 v[12:15], v[148:151], v[216:219], v[12:15]
	v_mfma_f32_16x16x32_bf16 v[16:19], v[120:123], v[206:209], v[16:19]
	v_mfma_f32_16x16x32_bf16 v[16:19], v[132:135], v[216:219], v[16:19]
	s_barrier
; #define PG8_MMA(ai, bj, At, Bt) do { __builtin_amdgcn_s_setprio(1); _Pragma("unroll") for (int m = 0; m < 4; ++m) _Pragma("unroll") for (int n = 0; n < 2; ++n) _Pragma("unroll") for (int k = 0; k < 2; ++k) \
;         acc[ai][bj][m][n] = __builtin_amdgcn_mfma_f32_16x16x32_bf16(Bt[n][k], At[m][k], acc[ai][bj][m][n], 0, 0, 0); __builtin_amdgcn_s_setprio(0); } while (0)
; #define PG8_WAIT_V(n) asm volatile("s_waitcnt vmcnt(" #n ")" ::: "memory")
; #define PG8_TRIP_HEAD(T) const int t = (T); const bool last = (t == nt - 2); \
;             const char* a1 = cA + (size_t)(t + 1) * kstep; \
;             const char* a2 = last ? nA : cA + (size_t)(t + 2) * kstep; const char* b2 = last ? nB : cB + (size_t)(t + 2) * kstep; \
;             const char* a3 = a2 + kstep; const char* b3 = b2 + kstep; \
;             if (last && has_next) S.a_ready(nxt);
; template <class Epi, class Sched, bool ALIGN_EPI = false, bool SP2 = false>
; __device__ __forceinline__ void gemm_phase(PG8_LAS unsigned char* lds, const Gemm g, const Sched& S, const Epi& E) {
;     ...
;         if constexpr (SP2) {
;             { PG8_TRIP_HEAD(0) PG8_TRIP_SP2(asm volatile("s_waitcnt vmcnt(%0)" :: "n"(8 + Epi::NST) : "memory"), PG8_MMAZ) }
;             for (int tt = 2; tt < nt; tt += 2) { PG8_TRIP_HEAD(tt) PG8_TRIP_SP2(PG8_WAIT_V(8), PG8_MMA) }
	ds_read_b128 v[120:123], v118
	ds_read_b128 v[132:135], v118 offset:1024
	ds_read_b128 v[144:147], v118 offset:2048
	ds_read_b128 v[148:151], v118 offset:3072
	ds_read_b128 v[152:155], v119
	ds_read_b128 v[156:159], v119 offset:1024
	ds_read_b128 v[166:169], v119 offset:2048
	ds_read_b128 v[170:173], v119 offset:3072
	s_mov_b32 m0, s35
	ds_read_b128 v[180:183], v178 offset:32768
	ds_read_b128 v[184:187], v178 offset:33792
	ds_read_b128 v[190:193], v178 offset:34816
	ds_read_b128 v[194:197], v178 offset:35840
	ds_read_b128 v[198:201], v178 offset:36864
	ds_read_b128 v[202:205], v178 offset:37888
	ds_read_b128 v[206:209], v178 offset:38912
	ds_read_b128 v[216:219], v178 offset:39936
	s_add_u32 s70, s50, s54
	s_addc_u32 s71, s51, s55
	global_load_lds_dwordx4 v160, s[70:71]
	s_mov_b32 m0, s36
	s_add_u32 s70, s50, s56
	s_addc_u32 s71, s51, s57
	global_load_lds_dwordx4 v160, s[70:71]
	s_waitcnt vmcnt(8) lgkmcnt(0)
	s_barrier
	v_mfma_f32_16x16x32_bf16 v[140:143], v[120:123], v[180:183], v[140:143]
	v_mfma_f32_16x16x32_bf16 v[140:143], v[132:135], v[184:187], v[140:143]
	v_mfma_f32_16x16x32_bf16 v[136:139], v[144:147], v[180:183], v[136:139]
	v_mfma_f32_16x16x32_bf16 v[136:139], v[148:151], v[184:187], v[136:139]
	v_mfma_f32_16x16x32_bf16 v[128:131], v[152:155], v[180:183], v[128:131]
	v_mfma_f32_16x16x32_bf16 v[128:131], v[156:159], v[184:187], v[128:131]
	v_mfma_f32_16x16x32_bf16 v[124:127], v[166:169], v[180:183], v[124:127]
	v_mfma_f32_16x16x32_bf16 v[124:127], v[170:173], v[184:187], v[124:127]
	v_mfma_f32_16x16x32_bf16 v[100:103], v[166:169], v[190:193], v[100:103]
	v_mfma_f32_16x16x32_bf16 v[100:103], v[170:173], v[194:197], v[100:103]
	v_mfma_f32_16x16x32_bf16 v[104:107], v[152:155], v[190:193], v[104:107]
	v_mfma_f32_16x16x32_bf16 v[104:107], v[156:159], v[194:197], v[104:107]
	v_mfma_f32_16x16x32_bf16 v[108:111], v[144:147], v[190:193], v[108:111]
	v_mfma_f32_16x16x32_bf16 v[108:111], v[148:151], v[194:197], v[108:111]
	v_mfma_f32_16x16x32_bf16 v[112:115], v[120:123], v[190:193], v[112:115]
	v_mfma_f32_16x16x32_bf16 v[112:115], v[132:135], v[194:197], v[112:115]
	v_mfma_f32_16x16x32_bf16 v[96:99], v[120:123], v[198:201], v[96:99]
	v_mfma_f32_16x16x32_bf16 v[96:99], v[132:135], v[202:205], v[96:99]
	v_mfma_f32_16x16x32_bf16 v[92:95], v[144:147], v[198:201], v[92:95]
	v_mfma_f32_16x16x32_bf16 v[92:95], v[148:151], v[202:205], v[92:95]
	v_mfma_f32_16x16x32_bf16 v[88:91], v[152:155], v[198:201], v[88:91]
	v_mfma_f32_16x16x32_bf16 v[88:91], v[156:159], v[202:205], v[88:91]
	v_mfma_f32_16x16x32_bf16 v[84:87], v[166:169], v[198:201], v[84:87]
	v_mfma_f32_16x16x32_bf16 v[84:87], v[170:173], v[202:205], v[84:87]
	v_mfma_f32_16x16x32_bf16 v[68:71], v[166:169], v[206:209], v[68:71]
	v_mfma_f32_16x16x32_bf16 v[68:71], v[170:173], v[216:219], v[68:71]
	v_mfma_f32_16x16x32_bf16 v[72:75], v[152:155], v[206:209], v[72:75]
	v_mfma_f32_16x16x32_bf16 v[72:75], v[156:159], v[216:219], v[72:75]
	v_mfma_f32_16x16x32_bf16 v[76:79], v[144:147], v[206:209], v[76:79]
	v_mfma_f32_16x16x32_bf16 v[76:79], v[148:151], v[216:219], v[76:79]
	v_mfma_f32_16x16x32_bf16 v[80:83], v[120:123], v[206:209], v[80:83]
	v_mfma_f32_16x16x32_bf16 v[80:83], v[132:135], v[216:219], v[80:83]
	s_barrier
	s_mov_b32 m0, s44
	ds_read_b128 v[180:183], v178 offset:49152
	ds_read_b128 v[184:187], v178 offset:50176
	ds_read_b128 v[190:193], v178 offset:51200
	ds_read_b128 v[194:197], v178 offset:52224
	ds_read_b128 v[198:201], v178 offset:53248
	ds_read_b128 v[202:205], v178 offset:54272
	ds_read_b128 v[206:209], v178 offset:55296
	ds_read_b128 v[216:219], v178 offset:56320
	s_add_u32 s70, s52, s78
	s_addc_u32 s71, s53, s79
	global_load_lds_dwordx4 v162, s[70:71]
	s_mov_b32 m0, s45
	s_add_u32 s70, s52, s60
	s_addc_u32 s71, s53, s61
	global_load_lds_dwordx4 v162, s[70:71]
	s_mov_b32 m0, s46
	s_add_u32 s70, s52, s62
	s_addc_u32 s71, s53, s63
	global_load_lds_dwordx4 v162, s[70:71]
	s_mov_b32 m0, s47
	s_add_u32 s70, s52, s64
	s_addc_u32 s71, s53, s65
	global_load_lds_dwordx4 v162, s[70:71]
	s_mov_b32 m0, s37
	s_add_u32 s70, s50, s78
	s_addc_u32 s71, s51, s79
	global_load_lds_dwordx4 v160, s[70:71]
	s_mov_b32 m0, s38
	s_add_u32 s70, s50, s60
	s_addc_u32 s71, s51, s61
	global_load_lds_dwordx4 v160, s[70:71]
	s_waitcnt vmcnt(8) lgkmcnt(0)
	s_barrier
	v_mfma_f32_16x16x32_bf16 v[56:59], v[120:123], v[180:183], v[56:59]
	v_mfma_f32_16x16x32_bf16 v[56:59], v[132:135], v[184:187], v[56:59]
	v_mfma_f32_16x16x32_bf16 v[52:55], v[144:147], v[180:183], v[52:55]
	v_mfma_f32_16x16x32_bf16 v[52:55], v[148:151], v[184:187], v[52:55]
	v_mfma_f32_16x16x32_bf16 v[64:67], v[152:155], v[180:183], v[64:67]
	v_mfma_f32_16x16x32_bf16 v[64:67], v[156:159], v[184:187], v[64:67]
	v_mfma_f32_16x16x32_bf16 v[60:63], v[166:169], v[180:183], v[60:63]
	v_mfma_f32_16x16x32_bf16 v[60:63], v[170:173], v[184:187], v[60:63]
	v_mfma_f32_16x16x32_bf16 v[36:39], v[166:169], v[190:193], v[36:39]
	v_mfma_f32_16x16x32_bf16 v[36:39], v[170:173], v[194:197], v[36:39]
	v_mfma_f32_16x16x32_bf16 v[40:43], v[152:155], v[190:193], v[40:43]
	v_mfma_f32_16x16x32_bf16 v[40:43], v[156:159], v[194:197], v[40:43]
	v_mfma_f32_16x16x32_bf16 v[44:47], v[144:147], v[190:193], v[44:47]
	v_mfma_f32_16x16x32_bf16 v[44:47], v[148:151], v[194:197], v[44:47]
	v_mfma_f32_16x16x32_bf16 v[48:51], v[120:123], v[190:193], v[48:51]
	v_mfma_f32_16x16x32_bf16 v[48:51], v[132:135], v[194:197], v[48:51]
	v_mfma_f32_16x16x32_bf16 v[32:35], v[120:123], v[198:201], v[32:35]
	v_mfma_f32_16x16x32_bf16 v[32:35], v[132:135], v[202:205], v[32:35]
	v_mfma_f32_16x16x32_bf16 v[28:31], v[144:147], v[198:201], v[28:31]
	v_mfma_f32_16x16x32_bf16 v[28:31], v[148:151], v[202:205], v[28:31]
	v_mfma_f32_16x16x32_bf16 v[24:27], v[152:155], v[198:201], v[24:27]
	v_mfma_f32_16x16x32_bf16 v[24:27], v[156:159], v[202:205], v[24:27]
	v_mfma_f32_16x16x32_bf16 v[20:23], v[166:169], v[198:201], v[20:23]
	v_mfma_f32_16x16x32_bf16 v[20:23], v[170:173], v[202:205], v[20:23]
	v_mfma_f32_16x16x32_bf16 v[4:7], v[166:169], v[206:209], v[4:7]
	v_mfma_f32_16x16x32_bf16 v[4:7], v[170:173], v[216:219], v[4:7]
	v_mfma_f32_16x16x32_bf16 v[8:11], v[152:155], v[206:209], v[8:11]
	v_mfma_f32_16x16x32_bf16 v[8:11], v[156:159], v[216:219], v[8:11]
	v_mfma_f32_16x16x32_bf16 v[12:15], v[144:147], v[206:209], v[12:15]
	v_mfma_f32_16x16x32_bf16 v[12:15], v[148:151], v[216:219], v[12:15]
	v_mfma_f32_16x16x32_bf16 v[16:19], v[120:123], v[206:209], v[16:19]
	v_mfma_f32_16x16x32_bf16 v[16:19], v[132:135], v[216:219], v[16:19]
	s_barrier
	s_add_i32 s48, s48, 2
	s_add_u32 s26, s26, 0x100
	s_addc_u32 s27, s27, 0
	s_add_u32 s24, s24, 0x100
	s_addc_u32 s25, s25, 0
	s_cmpk_gt_u32 s48, 0x55
	s_cbranch_scc0 .LBB0_233
	s_and_b64 vcc, exec, s[18:19]
	s_cbranch_vccz .LBB0_236
	s_barrier

.LBB0_324:
	ds_read_b128 v[136:139], v132
	ds_read_b128 v[140:143], v132 offset:1024
	ds_read_b128 v[144:147], v132 offset:2048
	ds_read_b128 v[148:151], v132 offset:3072
	ds_read_b128 v[152:155], v133
	ds_read_b128 v[156:159], v133 offset:1024
	ds_read_b128 v[160:163], v133 offset:2048
	ds_read_b128 v[174:177], v133 offset:3072
	s_add_u32 s15, s10, 0xfff7c080
	s_addc_u32 s50, s11, -1
	s_cmp_eq_u32 s14, 28
	s_cselect_b32 s51, s25, s50
	s_cselect_b32 s50, s24, s15
	s_cselect_b32 s53, s3, s13
	s_cselect_b32 s52, s4, s12
	s_mov_b32 m0, s5
	ds_read_b128 v[178:181], v200
	ds_read_b128 v[182:185], v200 offset:1024
	ds_read_b128 v[186:189], v200 offset:2048
	ds_read_b128 v[190:193], v200 offset:3072
	ds_read_b128 v[202:205], v200 offset:4096
	ds_read_b128 v[206:209], v200 offset:5120
	ds_read_b128 v[216:219], v200 offset:6144
	ds_read_b128 v[220:223], v200 offset:7168
	global_load_lds_dwordx4 v172, s[10:11]
	s_mov_b32 m0, s23
	s_add_u32 s70, s10, s96
	s_addc_u32 s71, s11, s97
	global_load_lds_dwordx4 v172, s[70:71]
	s_waitcnt vmcnt(8) lgkmcnt(0)
	s_barrier
	v_mfma_f32_16x16x32_bf16 v[120:123], v[136:139], v[178:181], v[120:123]
	v_mfma_f32_16x16x32_bf16 v[120:123], v[140:143], v[182:185], v[120:123]
	v_mfma_f32_16x16x32_bf16 v[116:119], v[144:147], v[178:181], v[116:119]
	v_mfma_f32_16x16x32_bf16 v[116:119], v[148:151], v[182:185], v[116:119]
	v_mfma_f32_16x16x32_bf16 v[128:131], v[152:155], v[178:181], v[128:131]
	v_mfma_f32_16x16x32_bf16 v[128:131], v[156:159], v[182:185], v[128:131]
	v_mfma_f32_16x16x32_bf16 v[124:127], v[160:163], v[178:181], v[124:127]
	v_mfma_f32_16x16x32_bf16 v[124:127], v[174:177], v[182:185], v[124:127]
	v_mfma_f32_16x16x32_bf16 v[108:111], v[160:163], v[186:189], v[108:111]
	v_mfma_f32_16x16x32_bf16 v[108:111], v[174:177], v[190:193], v[108:111]
	v_mfma_f32_16x16x32_bf16 v[112:115], v[152:155], v[186:189], v[112:115]
	v_mfma_f32_16x16x32_bf16 v[112:115], v[156:159], v[190:193], v[112:115]
	v_mfma_f32_16x16x32_bf16 v[100:103], v[144:147], v[186:189], v[100:103]
	v_mfma_f32_16x16x32_bf16 v[100:103], v[148:151], v[190:193], v[100:103]
	v_mfma_f32_16x16x32_bf16 v[104:107], v[136:139], v[186:189], v[104:107]
	v_mfma_f32_16x16x32_bf16 v[104:107], v[140:143], v[190:193], v[104:107]
	v_mfma_f32_16x16x32_bf16 v[88:91], v[136:139], v[202:205], v[88:91]
	v_mfma_f32_16x16x32_bf16 v[88:91], v[140:143], v[206:209], v[88:91]
	v_mfma_f32_16x16x32_bf16 v[84:87], v[144:147], v[202:205], v[84:87]
	v_mfma_f32_16x16x32_bf16 v[84:87], v[148:151], v[206:209], v[84:87]
	v_mfma_f32_16x16x32_bf16 v[96:99], v[152:155], v[202:205], v[96:99]
	v_mfma_f32_16x16x32_bf16 v[96:99], v[156:159], v[206:209], v[96:99]
	v_mfma_f32_16x16x32_bf16 v[92:95], v[160:163], v[202:205], v[92:95]
	v_mfma_f32_16x16x32_bf16 v[92:95], v[174:177], v[206:209], v[92:95]
	v_mfma_f32_16x16x32_bf16 v[76:79], v[160:163], v[216:219], v[76:79]
	v_mfma_f32_16x16x32_bf16 v[76:79], v[174:177], v[220:223], v[76:79]
	v_mfma_f32_16x16x32_bf16 v[80:83], v[152:155], v[216:219], v[80:83]
	v_mfma_f32_16x16x32_bf16 v[80:83], v[156:159], v[220:223], v[80:83]
	v_mfma_f32_16x16x32_bf16 v[68:71], v[144:147], v[216:219], v[68:71]
	v_mfma_f32_16x16x32_bf16 v[68:71], v[148:151], v[220:223], v[68:71]
	v_mfma_f32_16x16x32_bf16 v[72:75], v[136:139], v[216:219], v[72:75]
	v_mfma_f32_16x16x32_bf16 v[72:75], v[140:143], v[220:223], v[72:75]
	s_barrier
	s_mov_b32 m0, s28
	ds_read_b128 v[178:181], v200 offset:16384
	ds_read_b128 v[182:185], v200 offset:17408
	ds_read_b128 v[186:189], v200 offset:18432
	ds_read_b128 v[190:193], v200 offset:19456
	ds_read_b128 v[202:205], v200 offset:20480
	ds_read_b128 v[206:209], v200 offset:21504
	ds_read_b128 v[216:219], v200 offset:22528
	ds_read_b128 v[220:223], v200 offset:23552
	global_load_lds_dwordx4 v164, s[52:53]
	s_mov_b32 m0, s29
	s_add_u32 s70, s52, s90
	s_addc_u32 s71, s53, s91
	global_load_lds_dwordx4 v164, s[70:71]
	s_mov_b32 m0, s33
	s_add_u32 s70, s52, s54
	s_addc_u32 s71, s53, s55
	global_load_lds_dwordx4 v164, s[70:71]
	s_mov_b32 m0, s45
	s_add_u32 s70, s52, s60
	s_addc_u32 s71, s53, s61
	global_load_lds_dwordx4 v164, s[70:71]
	s_mov_b32 m0, s30
	s_nop 0
	global_load_lds_dwordx4 v166, s[50:51]
	s_mov_b32 m0, s31
	s_add_u32 s70, s50, s96
	s_addc_u32 s71, s51, s97
	global_load_lds_dwordx4 v166, s[70:71]
	s_waitcnt vmcnt(8) lgkmcnt(0)
	s_barrier
	v_mfma_f32_16x16x32_bf16 v[56:59], v[136:139], v[178:181], v[56:59]
	v_mfma_f32_16x16x32_bf16 v[56:59], v[140:143], v[182:185], v[56:59]
	v_mfma_f32_16x16x32_bf16 v[52:55], v[144:147], v[178:181], v[52:55]
	v_mfma_f32_16x16x32_bf16 v[52:55], v[148:151], v[182:185], v[52:55]
	v_mfma_f32_16x16x32_bf16 v[64:67], v[152:155], v[178:181], v[64:67]
	v_mfma_f32_16x16x32_bf16 v[64:67], v[156:159], v[182:185], v[64:67]
	v_mfma_f32_16x16x32_bf16 v[60:63], v[160:163], v[178:181], v[60:63]
	v_mfma_f32_16x16x32_bf16 v[60:63], v[174:177], v[182:185], v[60:63]
	v_mfma_f32_16x16x32_bf16 v[44:47], v[160:163], v[186:189], v[44:47]
	v_mfma_f32_16x16x32_bf16 v[44:47], v[174:177], v[190:193], v[44:47]
	v_mfma_f32_16x16x32_bf16 v[48:51], v[152:155], v[186:189], v[48:51]
	v_mfma_f32_16x16x32_bf16 v[48:51], v[156:159], v[190:193], v[48:51]
	v_mfma_f32_16x16x32_bf16 v[36:39], v[144:147], v[186:189], v[36:39]
	v_mfma_f32_16x16x32_bf16 v[36:39], v[148:151], v[190:193], v[36:39]
	v_mfma_f32_16x16x32_bf16 v[40:43], v[136:139], v[186:189], v[40:43]
	v_mfma_f32_16x16x32_bf16 v[40:43], v[140:143], v[190:193], v[40:43]
	v_mfma_f32_16x16x32_bf16 v[24:27], v[136:139], v[202:205], v[24:27]
	v_mfma_f32_16x16x32_bf16 v[24:27], v[140:143], v[206:209], v[24:27]
	v_mfma_f32_16x16x32_bf16 v[20:23], v[144:147], v[202:205], v[20:23]
	v_mfma_f32_16x16x32_bf16 v[20:23], v[148:151], v[206:209], v[20:23]
	v_mfma_f32_16x16x32_bf16 v[32:35], v[152:155], v[202:205], v[32:35]
	v_mfma_f32_16x16x32_bf16 v[32:35], v[156:159], v[206:209], v[32:35]
	v_mfma_f32_16x16x32_bf16 v[28:31], v[160:163], v[202:205], v[28:31]
	v_mfma_f32_16x16x32_bf16 v[28:31], v[174:177], v[206:209], v[28:31]
	v_mfma_f32_16x16x32_bf16 v[12:15], v[160:163], v[216:219], v[12:15]
	v_mfma_f32_16x16x32_bf16 v[12:15], v[174:177], v[220:223], v[12:15]
	v_mfma_f32_16x16x32_bf16 v[16:19], v[152:155], v[216:219], v[16:19]
	v_mfma_f32_16x16x32_bf16 v[16:19], v[156:159], v[220:223], v[16:19]
	v_mfma_f32_16x16x32_bf16 v[4:7], v[144:147], v[216:219], v[4:7]
	v_mfma_f32_16x16x32_bf16 v[4:7], v[148:151], v[220:223], v[4:7]
	v_mfma_f32_16x16x32_bf16 v[8:11], v[136:139], v[216:219], v[8:11]
	v_mfma_f32_16x16x32_bf16 v[8:11], v[140:143], v[220:223], v[8:11]
	s_barrier
; #define PG8_MMA(ai, bj, At, Bt) do { __builtin_amdgcn_s_setprio(1); _Pragma("unroll") for (int m = 0; m < 4; ++m) _Pragma("unroll") for (int n = 0; n < 2; ++n) _Pragma("unroll") for (int k = 0; k < 2; ++k) \
;         acc[ai][bj][m][n] = __builtin_amdgcn_mfma_f32_16x16x32_bf16(Bt[n][k], At[m][k], acc[ai][bj][m][n], 0, 0, 0); __builtin_amdgcn_s_setprio(0); } while (0)
; #define PG8_WAIT_V(n) asm volatile("s_waitcnt vmcnt(" #n ")" ::: "memory")
; #define PG8_TRIP_HEAD(T) const int t = (T); const bool last = (t == nt - 2); \
;             const char* a1 = cA + (size_t)(t + 1) * kstep; \
;             const char* a2 = last ? nA : cA + (size_t)(t + 2) * kstep; const char* b2 = last ? nB : cB + (size_t)(t + 2) * kstep; \
;             const char* a3 = a2 + kstep; const char* b3 = b2 + kstep; \
;             if (last && has_next) S.a_ready(nxt);
; template <class Epi, class Sched, bool ALIGN_EPI = false, bool SP2 = false>
; __device__ __forceinline__ void gemm_phase(PG8_LAS unsigned char* lds, const Gemm g, const Sched& S, const Epi& E) {
;     ...
;         if constexpr (SP2) {
;             { PG8_TRIP_HEAD(0) PG8_TRIP_SP2(asm volatile("s_waitcnt vmcnt(%0)" :: "n"(8 + Epi::NST) : "memory"), PG8_MMAZ) }
;             for (int tt = 2; tt < nt; tt += 2) { PG8_TRIP_HEAD(tt) PG8_TRIP_SP2(PG8_WAIT_V(8), PG8_MMA) }
	ds_read_b128 v[136:139], v134
	ds_read_b128 v[140:143], v134 offset:1024
	ds_read_b128 v[144:147], v134 offset:2048
	ds_read_b128 v[148:151], v134 offset:3072
	ds_read_b128 v[152:155], v135
	ds_read_b128 v[156:159], v135 offset:1024
	ds_read_b128 v[160:163], v135 offset:2048
	ds_read_b128 v[174:177], v135 offset:3072
	s_mov_b32 m0, s34
	ds_read_b128 v[178:181], v200 offset:32768
	ds_read_b128 v[182:185], v200 offset:33792
	ds_read_b128 v[186:189], v200 offset:34816
	ds_read_b128 v[190:193], v200 offset:35840
	ds_read_b128 v[202:205], v200 offset:36864
	ds_read_b128 v[206:209], v200 offset:37888
	ds_read_b128 v[216:219], v200 offset:38912
	ds_read_b128 v[220:223], v200 offset:39936
	s_add_u32 s70, s50, s82
	s_addc_u32 s71, s51, s83
	global_load_lds_dwordx4 v166, s[70:71]
	s_mov_b32 m0, s35
	s_add_u32 s70, s50, s64
	s_addc_u32 s71, s51, s65
	global_load_lds_dwordx4 v166, s[70:71]
	s_waitcnt vmcnt(8) lgkmcnt(0)
	s_barrier
	v_mfma_f32_16x16x32_bf16 v[120:123], v[136:139], v[178:181], v[120:123]
	v_mfma_f32_16x16x32_bf16 v[120:123], v[140:143], v[182:185], v[120:123]
	v_mfma_f32_16x16x32_bf16 v[116:119], v[144:147], v[178:181], v[116:119]
	v_mfma_f32_16x16x32_bf16 v[116:119], v[148:151], v[182:185], v[116:119]
	v_mfma_f32_16x16x32_bf16 v[128:131], v[152:155], v[178:181], v[128:131]
	v_mfma_f32_16x16x32_bf16 v[128:131], v[156:159], v[182:185], v[128:131]
	v_mfma_f32_16x16x32_bf16 v[124:127], v[160:163], v[178:181], v[124:127]
	v_mfma_f32_16x16x32_bf16 v[124:127], v[174:177], v[182:185], v[124:127]
	v_mfma_f32_16x16x32_bf16 v[108:111], v[160:163], v[186:189], v[108:111]
	v_mfma_f32_16x16x32_bf16 v[108:111], v[174:177], v[190:193], v[108:111]
	v_mfma_f32_16x16x32_bf16 v[112:115], v[152:155], v[186:189], v[112:115]
	v_mfma_f32_16x16x32_bf16 v[112:115], v[156:159], v[190:193], v[112:115]
	v_mfma_f32_16x16x32_bf16 v[100:103], v[144:147], v[186:189], v[100:103]
	v_mfma_f32_16x16x32_bf16 v[100:103], v[148:151], v[190:193], v[100:103]
	v_mfma_f32_16x16x32_bf16 v[104:107], v[136:139], v[186:189], v[104:107]
	v_mfma_f32_16x16x32_bf16 v[104:107], v[140:143], v[190:193], v[104:107]
	v_mfma_f32_16x16x32_bf16 v[88:91], v[136:139], v[202:205], v[88:91]
	v_mfma_f32_16x16x32_bf16 v[88:91], v[140:143], v[206:209], v[88:91]
	v_mfma_f32_16x16x32_bf16 v[84:87], v[144:147], v[202:205], v[84:87]
	v_mfma_f32_16x16x32_bf16 v[84:87], v[148:151], v[206:209], v[84:87]
	v_mfma_f32_16x16x32_bf16 v[96:99], v[152:155], v[202:205], v[96:99]
	v_mfma_f32_16x16x32_bf16 v[96:99], v[156:159], v[206:209], v[96:99]
	v_mfma_f32_16x16x32_bf16 v[92:95], v[160:163], v[202:205], v[92:95]
	v_mfma_f32_16x16x32_bf16 v[92:95], v[174:177], v[206:209], v[92:95]
	v_mfma_f32_16x16x32_bf16 v[76:79], v[160:163], v[216:219], v[76:79]
	v_mfma_f32_16x16x32_bf16 v[76:79], v[174:177], v[220:223], v[76:79]
	v_mfma_f32_16x16x32_bf16 v[80:83], v[152:155], v[216:219], v[80:83]
	v_mfma_f32_16x16x32_bf16 v[80:83], v[156:159], v[220:223], v[80:83]
	v_mfma_f32_16x16x32_bf16 v[68:71], v[144:147], v[216:219], v[68:71]
	v_mfma_f32_16x16x32_bf16 v[68:71], v[148:151], v[220:223], v[68:71]
	v_mfma_f32_16x16x32_bf16 v[72:75], v[136:139], v[216:219], v[72:75]
	v_mfma_f32_16x16x32_bf16 v[72:75], v[140:143], v[220:223], v[72:75]
	s_barrier
	s_mov_b32 m0, s46
	ds_read_b128 v[178:181], v200 offset:49152
	ds_read_b128 v[182:185], v200 offset:50176
	ds_read_b128 v[186:189], v200 offset:51200
	ds_read_b128 v[190:193], v200 offset:52224
	ds_read_b128 v[202:205], v200 offset:53248
	ds_read_b128 v[206:209], v200 offset:54272
	ds_read_b128 v[216:219], v200 offset:55296
	ds_read_b128 v[220:223], v200 offset:56320
	s_add_u32 s70, s52, s78
	s_addc_u32 s71, s53, s79
	global_load_lds_dwordx4 v164, s[70:71]
	s_mov_b32 m0, s47
	s_add_u32 s70, s52, s84
	s_addc_u32 s71, s53, s85
	global_load_lds_dwordx4 v164, s[70:71]
	s_mov_b32 m0, s48
	s_add_u32 s70, s52, s56
	s_addc_u32 s71, s53, s57
	global_load_lds_dwordx4 v164, s[70:71]
	s_mov_b32 m0, s49
	s_add_u32 s70, s52, s62
	s_addc_u32 s71, s53, s63
	global_load_lds_dwordx4 v164, s[70:71]
	s_mov_b32 m0, s38
	s_add_u32 s70, s50, s78
	s_addc_u32 s71, s51, s79
	global_load_lds_dwordx4 v166, s[70:71]
	s_mov_b32 m0, s39
	s_add_u32 s70, s50, s92
	s_addc_u32 s71, s51, s93
	global_load_lds_dwordx4 v166, s[70:71]
	s_waitcnt vmcnt(8) lgkmcnt(0)
	s_barrier
	v_mfma_f32_16x16x32_bf16 v[56:59], v[136:139], v[178:181], v[56:59]
	v_mfma_f32_16x16x32_bf16 v[56:59], v[140:143], v[182:185], v[56:59]
	v_mfma_f32_16x16x32_bf16 v[52:55], v[144:147], v[178:181], v[52:55]
	v_mfma_f32_16x16x32_bf16 v[52:55], v[148:151], v[182:185], v[52:55]
	v_mfma_f32_16x16x32_bf16 v[64:67], v[152:155], v[178:181], v[64:67]
	v_mfma_f32_16x16x32_bf16 v[64:67], v[156:159], v[182:185], v[64:67]
	v_mfma_f32_16x16x32_bf16 v[60:63], v[160:163], v[178:181], v[60:63]
	v_mfma_f32_16x16x32_bf16 v[60:63], v[174:177], v[182:185], v[60:63]
	v_mfma_f32_16x16x32_bf16 v[44:47], v[160:163], v[186:189], v[44:47]
	v_mfma_f32_16x16x32_bf16 v[44:47], v[174:177], v[190:193], v[44:47]
	v_mfma_f32_16x16x32_bf16 v[48:51], v[152:155], v[186:189], v[48:51]
	v_mfma_f32_16x16x32_bf16 v[48:51], v[156:159], v[190:193], v[48:51]
	v_mfma_f32_16x16x32_bf16 v[36:39], v[144:147], v[186:189], v[36:39]
	v_mfma_f32_16x16x32_bf16 v[36:39], v[148:151], v[190:193], v[36:39]
	v_mfma_f32_16x16x32_bf16 v[40:43], v[136:139], v[186:189], v[40:43]
	v_mfma_f32_16x16x32_bf16 v[40:43], v[140:143], v[190:193], v[40:43]
	v_mfma_f32_16x16x32_bf16 v[24:27], v[136:139], v[202:205], v[24:27]
	v_mfma_f32_16x16x32_bf16 v[24:27], v[140:143], v[206:209], v[24:27]
	v_mfma_f32_16x16x32_bf16 v[20:23], v[144:147], v[202:205], v[20:23]
	v_mfma_f32_16x16x32_bf16 v[20:23], v[148:151], v[206:209], v[20:23]
	v_mfma_f32_16x16x32_bf16 v[32:35], v[152:155], v[202:205], v[32:35]
	v_mfma_f32_16x16x32_bf16 v[32:35], v[156:159], v[206:209], v[32:35]
	v_mfma_f32_16x16x32_bf16 v[28:31], v[160:163], v[202:205], v[28:31]
	v_mfma_f32_16x16x32_bf16 v[28:31], v[174:177], v[206:209], v[28:31]
	v_mfma_f32_16x16x32_bf16 v[12:15], v[160:163], v[216:219], v[12:15]
	v_mfma_f32_16x16x32_bf16 v[12:15], v[174:177], v[220:223], v[12:15]
	v_mfma_f32_16x16x32_bf16 v[16:19], v[152:155], v[216:219], v[16:19]
	v_mfma_f32_16x16x32_bf16 v[16:19], v[156:159], v[220:223], v[16:19]
	v_mfma_f32_16x16x32_bf16 v[4:7], v[144:147], v[216:219], v[4:7]
	v_mfma_f32_16x16x32_bf16 v[4:7], v[148:151], v[220:223], v[4:7]
	v_mfma_f32_16x16x32_bf16 v[8:11], v[136:139], v[216:219], v[8:11]
	v_mfma_f32_16x16x32_bf16 v[8:11], v[140:143], v[220:223], v[8:11]
	s_barrier
	s_add_i32 s14, s14, 2
	s_add_u32 s10, s10, 0x100
	s_addc_u32 s11, s11, 0
	s_add_u32 s12, s12, 0x100
	s_addc_u32 s13, s13, 0
	s_cmp_gt_u32 s14, 29
	s_cbranch_scc0 .LBB0_324
	s_and_b64 vcc, exec, s[18:19]
	s_cbranch_vccz .LBB0_327
	s_barrier

.LBB0_594:
	ds_read_b128 v[136:139], v116
	ds_read_b128 v[140:143], v116 offset:1024
	ds_read_b128 v[144:147], v116 offset:2048
	ds_read_b128 v[148:151], v116 offset:3072
	ds_read_b128 v[152:155], v117
	ds_read_b128 v[156:159], v117 offset:1024
	ds_read_b128 v[160:163], v117 offset:2048
	ds_read_b128 v[164:167], v117 offset:3072
	s_add_u32 s43, s20, 0xfff7c080
	s_addc_u32 s44, s21, -1
	s_cmp_eq_u32 s15, 28
	s_cselect_b32 s45, s17, s44
	s_cselect_b32 s44, s16, s43
	s_cselect_b32 s47, s4, s9
	s_cselect_b32 s46, s5, s8
	s_mov_b32 m0, s33
	ds_read_b128 v[168:171], v221
	ds_read_b128 v[172:175], v221 offset:1024
	ds_read_b128 v[176:179], v221 offset:2048
	ds_read_b128 v[180:183], v221 offset:3072
	ds_read_b128 v[184:187], v221 offset:4096
	ds_read_b128 v[188:191], v221 offset:5120
	ds_read_b128 v[202:205], v221 offset:6144
	ds_read_b128 v[206:209], v221 offset:7168
	global_load_lds_dwordx4 v200, s[20:21]
	s_mov_b32 m0, s34
	s_add_u32 s70, s20, s96
	s_addc_u32 s71, s21, s97
	global_load_lds_dwordx4 v200, s[70:71]
	s_waitcnt vmcnt(8) lgkmcnt(0)
	s_barrier
	v_mfma_f32_16x16x32_bf16 v[130:133], v[136:139], v[168:171], v[130:133]
	v_mfma_f32_16x16x32_bf16 v[130:133], v[140:143], v[172:175], v[130:133]
	v_mfma_f32_16x16x32_bf16 v[126:129], v[144:147], v[168:171], v[126:129]
	v_mfma_f32_16x16x32_bf16 v[126:129], v[148:151], v[172:175], v[126:129]
	v_mfma_f32_16x16x32_bf16 v[122:125], v[152:155], v[168:171], v[122:125]
	v_mfma_f32_16x16x32_bf16 v[122:125], v[156:159], v[172:175], v[122:125]
	v_mfma_f32_16x16x32_bf16 v[118:121], v[160:163], v[168:171], v[118:121]
	v_mfma_f32_16x16x32_bf16 v[118:121], v[164:167], v[172:175], v[118:121]
	v_mfma_f32_16x16x32_bf16 v[100:103], v[160:163], v[176:179], v[100:103]
	v_mfma_f32_16x16x32_bf16 v[100:103], v[164:167], v[180:183], v[100:103]
	v_mfma_f32_16x16x32_bf16 v[104:107], v[152:155], v[176:179], v[104:107]
	v_mfma_f32_16x16x32_bf16 v[104:107], v[156:159], v[180:183], v[104:107]
	v_mfma_f32_16x16x32_bf16 v[108:111], v[144:147], v[176:179], v[108:111]
	v_mfma_f32_16x16x32_bf16 v[108:111], v[148:151], v[180:183], v[108:111]
	v_mfma_f32_16x16x32_bf16 v[112:115], v[136:139], v[176:179], v[112:115]
	v_mfma_f32_16x16x32_bf16 v[112:115], v[140:143], v[180:183], v[112:115]
	v_mfma_f32_16x16x32_bf16 v[96:99], v[136:139], v[184:187], v[96:99]
	v_mfma_f32_16x16x32_bf16 v[96:99], v[140:143], v[188:191], v[96:99]
	v_mfma_f32_16x16x32_bf16 v[92:95], v[144:147], v[184:187], v[92:95]
	v_mfma_f32_16x16x32_bf16 v[92:95], v[148:151], v[188:191], v[92:95]
	v_mfma_f32_16x16x32_bf16 v[88:91], v[152:155], v[184:187], v[88:91]
	v_mfma_f32_16x16x32_bf16 v[88:91], v[156:159], v[188:191], v[88:91]
	v_mfma_f32_16x16x32_bf16 v[84:87], v[160:163], v[184:187], v[84:87]
	v_mfma_f32_16x16x32_bf16 v[84:87], v[164:167], v[188:191], v[84:87]
	v_mfma_f32_16x16x32_bf16 v[68:71], v[160:163], v[202:205], v[68:71]
	v_mfma_f32_16x16x32_bf16 v[68:71], v[164:167], v[206:209], v[68:71]
	v_mfma_f32_16x16x32_bf16 v[72:75], v[152:155], v[202:205], v[72:75]
	v_mfma_f32_16x16x32_bf16 v[72:75], v[156:159], v[206:209], v[72:75]
	v_mfma_f32_16x16x32_bf16 v[76:79], v[144:147], v[202:205], v[76:79]
	v_mfma_f32_16x16x32_bf16 v[76:79], v[148:151], v[206:209], v[76:79]
	v_mfma_f32_16x16x32_bf16 v[80:83], v[136:139], v[202:205], v[80:83]
	v_mfma_f32_16x16x32_bf16 v[80:83], v[140:143], v[206:209], v[80:83]
	s_barrier
	s_mov_b32 m0, s35
	ds_read_b128 v[168:171], v221 offset:16384
	ds_read_b128 v[172:175], v221 offset:17408
	ds_read_b128 v[176:179], v221 offset:18432
	ds_read_b128 v[180:183], v221 offset:19456
	ds_read_b128 v[184:187], v221 offset:20480
	ds_read_b128 v[188:191], v221 offset:21504
	ds_read_b128 v[202:205], v221 offset:22528
	ds_read_b128 v[206:209], v221 offset:23552
	global_load_lds_dwordx4 v194, s[46:47]
	s_mov_b32 m0, s36
	s_add_u32 s70, s46, s90
	s_addc_u32 s71, s47, s91
	global_load_lds_dwordx4 v194, s[70:71]
	s_mov_b32 m0, s37
	s_add_u32 s70, s46, s48
	s_addc_u32 s71, s47, s49
	global_load_lds_dwordx4 v194, s[70:71]
	s_mov_b32 m0, s38
	s_add_u32 s70, s46, s52
	s_addc_u32 s71, s47, s53
	global_load_lds_dwordx4 v194, s[70:71]
	s_mov_b32 m0, s23
	s_nop 0
	global_load_lds_dwordx4 v196, s[44:45]
	s_mov_b32 m0, s24
	s_add_u32 s70, s44, s96
	s_addc_u32 s71, s45, s97
	global_load_lds_dwordx4 v196, s[70:71]
	s_waitcnt vmcnt(8) lgkmcnt(0)
	s_barrier
	v_mfma_f32_16x16x32_bf16 v[64:67], v[136:139], v[168:171], v[64:67]
	v_mfma_f32_16x16x32_bf16 v[64:67], v[140:143], v[172:175], v[64:67]
	v_mfma_f32_16x16x32_bf16 v[60:63], v[144:147], v[168:171], v[60:63]
	v_mfma_f32_16x16x32_bf16 v[60:63], v[148:151], v[172:175], v[60:63]
	v_mfma_f32_16x16x32_bf16 v[56:59], v[152:155], v[168:171], v[56:59]
	v_mfma_f32_16x16x32_bf16 v[56:59], v[156:159], v[172:175], v[56:59]
	v_mfma_f32_16x16x32_bf16 v[52:55], v[160:163], v[168:171], v[52:55]
	v_mfma_f32_16x16x32_bf16 v[52:55], v[164:167], v[172:175], v[52:55]
	v_mfma_f32_16x16x32_bf16 v[36:39], v[160:163], v[176:179], v[36:39]
	v_mfma_f32_16x16x32_bf16 v[36:39], v[164:167], v[180:183], v[36:39]
	v_mfma_f32_16x16x32_bf16 v[40:43], v[152:155], v[176:179], v[40:43]
	v_mfma_f32_16x16x32_bf16 v[40:43], v[156:159], v[180:183], v[40:43]
	v_mfma_f32_16x16x32_bf16 v[44:47], v[144:147], v[176:179], v[44:47]
	v_mfma_f32_16x16x32_bf16 v[44:47], v[148:151], v[180:183], v[44:47]
	v_mfma_f32_16x16x32_bf16 v[48:51], v[136:139], v[176:179], v[48:51]
	v_mfma_f32_16x16x32_bf16 v[48:51], v[140:143], v[180:183], v[48:51]
	v_mfma_f32_16x16x32_bf16 v[32:35], v[136:139], v[184:187], v[32:35]
	v_mfma_f32_16x16x32_bf16 v[32:35], v[140:143], v[188:191], v[32:35]
	v_mfma_f32_16x16x32_bf16 v[28:31], v[144:147], v[184:187], v[28:31]
	v_mfma_f32_16x16x32_bf16 v[28:31], v[148:151], v[188:191], v[28:31]
	v_mfma_f32_16x16x32_bf16 v[24:27], v[152:155], v[184:187], v[24:27]
	v_mfma_f32_16x16x32_bf16 v[24:27], v[156:159], v[188:191], v[24:27]
	v_mfma_f32_16x16x32_bf16 v[20:23], v[160:163], v[184:187], v[20:23]
	v_mfma_f32_16x16x32_bf16 v[20:23], v[164:167], v[188:191], v[20:23]
	v_mfma_f32_16x16x32_bf16 v[4:7], v[160:163], v[202:205], v[4:7]
	v_mfma_f32_16x16x32_bf16 v[4:7], v[164:167], v[206:209], v[4:7]
	v_mfma_f32_16x16x32_bf16 v[8:11], v[152:155], v[202:205], v[8:11]
	v_mfma_f32_16x16x32_bf16 v[8:11], v[156:159], v[206:209], v[8:11]
	v_mfma_f32_16x16x32_bf16 v[12:15], v[144:147], v[202:205], v[12:15]
	v_mfma_f32_16x16x32_bf16 v[12:15], v[148:151], v[206:209], v[12:15]
	v_mfma_f32_16x16x32_bf16 v[16:19], v[136:139], v[202:205], v[16:19]
	v_mfma_f32_16x16x32_bf16 v[16:19], v[140:143], v[206:209], v[16:19]
	s_barrier
; #define PG8_MMA(ai, bj, At, Bt) do { __builtin_amdgcn_s_setprio(1); _Pragma("unroll") for (int m = 0; m < 4; ++m) _Pragma("unroll") for (int n = 0; n < 2; ++n) _Pragma("unroll") for (int k = 0; k < 2; ++k) \
;         acc[ai][bj][m][n] = __builtin_amdgcn_mfma_f32_16x16x32_bf16(Bt[n][k], At[m][k], acc[ai][bj][m][n], 0, 0, 0); __builtin_amdgcn_s_setprio(0); } while (0)
; #define PG8_WAIT_V(n) asm volatile("s_waitcnt vmcnt(" #n ")" ::: "memory")
; #define PG8_TRIP_HEAD(T) const int t = (T); const bool last = (t == nt - 2); \
;             const char* a1 = cA + (size_t)(t + 1) * kstep; \
;             const char* a2 = last ? nA : cA + (size_t)(t + 2) * kstep; const char* b2 = last ? nB : cB + (size_t)(t + 2) * kstep; \
;             const char* a3 = a2 + kstep; const char* b3 = b2 + kstep; \
;             if (last && has_next) S.a_ready(nxt);
; template <class Epi, class Sched, bool ALIGN_EPI = false, bool SP2 = false>
; __device__ __forceinline__ void gemm_phase(PG8_LAS unsigned char* lds, const Gemm g, const Sched& S, const Epi& E) {
;     ...
;         if constexpr (SP2) {
;             { PG8_TRIP_HEAD(0) PG8_TRIP_SP2(asm volatile("s_waitcnt vmcnt(%0)" :: "n"(8 + Epi::NST) : "memory"), PG8_MMAZ) }
;             for (int tt = 2; tt < nt; tt += 2) { PG8_TRIP_HEAD(tt) PG8_TRIP_SP2(PG8_WAIT_V(8), PG8_MMA) }
	ds_read_b128 v[136:139], v134
	ds_read_b128 v[140:143], v134 offset:1024
	ds_read_b128 v[144:147], v134 offset:2048
	ds_read_b128 v[148:151], v134 offset:3072
	ds_read_b128 v[152:155], v135
	ds_read_b128 v[156:159], v135 offset:1024
	ds_read_b128 v[160:163], v135 offset:2048
	ds_read_b128 v[164:167], v135 offset:3072
	s_mov_b32 m0, s25
	ds_read_b128 v[168:171], v221 offset:32768
	ds_read_b128 v[172:175], v221 offset:33792
	ds_read_b128 v[176:179], v221 offset:34816
	ds_read_b128 v[180:183], v221 offset:35840
	ds_read_b128 v[184:187], v221 offset:36864
	ds_read_b128 v[188:191], v221 offset:37888
	ds_read_b128 v[202:205], v221 offset:38912
	ds_read_b128 v[206:209], v221 offset:39936
	s_add_u32 s70, s44, s82
	s_addc_u32 s71, s45, s83
	global_load_lds_dwordx4 v196, s[70:71]
	s_mov_b32 m0, s26
	s_add_u32 s70, s44, s56
	s_addc_u32 s71, s45, s57
	global_load_lds_dwordx4 v196, s[70:71]
	s_waitcnt vmcnt(8) lgkmcnt(0)
	s_barrier
	v_mfma_f32_16x16x32_bf16 v[130:133], v[136:139], v[168:171], v[130:133]
	v_mfma_f32_16x16x32_bf16 v[130:133], v[140:143], v[172:175], v[130:133]
	v_mfma_f32_16x16x32_bf16 v[126:129], v[144:147], v[168:171], v[126:129]
	v_mfma_f32_16x16x32_bf16 v[126:129], v[148:151], v[172:175], v[126:129]
	v_mfma_f32_16x16x32_bf16 v[122:125], v[152:155], v[168:171], v[122:125]
	v_mfma_f32_16x16x32_bf16 v[122:125], v[156:159], v[172:175], v[122:125]
	v_mfma_f32_16x16x32_bf16 v[118:121], v[160:163], v[168:171], v[118:121]
	v_mfma_f32_16x16x32_bf16 v[118:121], v[164:167], v[172:175], v[118:121]
	v_mfma_f32_16x16x32_bf16 v[100:103], v[160:163], v[176:179], v[100:103]
	v_mfma_f32_16x16x32_bf16 v[100:103], v[164:167], v[180:183], v[100:103]
	v_mfma_f32_16x16x32_bf16 v[104:107], v[152:155], v[176:179], v[104:107]
	v_mfma_f32_16x16x32_bf16 v[104:107], v[156:159], v[180:183], v[104:107]
	v_mfma_f32_16x16x32_bf16 v[108:111], v[144:147], v[176:179], v[108:111]
	v_mfma_f32_16x16x32_bf16 v[108:111], v[148:151], v[180:183], v[108:111]
	v_mfma_f32_16x16x32_bf16 v[112:115], v[136:139], v[176:179], v[112:115]
	v_mfma_f32_16x16x32_bf16 v[112:115], v[140:143], v[180:183], v[112:115]
	v_mfma_f32_16x16x32_bf16 v[96:99], v[136:139], v[184:187], v[96:99]
	v_mfma_f32_16x16x32_bf16 v[96:99], v[140:143], v[188:191], v[96:99]
	v_mfma_f32_16x16x32_bf16 v[92:95], v[144:147], v[184:187], v[92:95]
	v_mfma_f32_16x16x32_bf16 v[92:95], v[148:151], v[188:191], v[92:95]
	v_mfma_f32_16x16x32_bf16 v[88:91], v[152:155], v[184:187], v[88:91]
	v_mfma_f32_16x16x32_bf16 v[88:91], v[156:159], v[188:191], v[88:91]
	v_mfma_f32_16x16x32_bf16 v[84:87], v[160:163], v[184:187], v[84:87]
	v_mfma_f32_16x16x32_bf16 v[84:87], v[164:167], v[188:191], v[84:87]
	v_mfma_f32_16x16x32_bf16 v[68:71], v[160:163], v[202:205], v[68:71]
	v_mfma_f32_16x16x32_bf16 v[68:71], v[164:167], v[206:209], v[68:71]
	v_mfma_f32_16x16x32_bf16 v[72:75], v[152:155], v[202:205], v[72:75]
	v_mfma_f32_16x16x32_bf16 v[72:75], v[156:159], v[206:209], v[72:75]
	v_mfma_f32_16x16x32_bf16 v[76:79], v[144:147], v[202:205], v[76:79]
	v_mfma_f32_16x16x32_bf16 v[76:79], v[148:151], v[206:209], v[76:79]
	v_mfma_f32_16x16x32_bf16 v[80:83], v[136:139], v[202:205], v[80:83]
	v_mfma_f32_16x16x32_bf16 v[80:83], v[140:143], v[206:209], v[80:83]
	s_barrier
	s_mov_b32 m0, s39
	ds_read_b128 v[168:171], v221 offset:49152
	ds_read_b128 v[172:175], v221 offset:50176
	ds_read_b128 v[176:179], v221 offset:51200
	ds_read_b128 v[180:183], v221 offset:52224
	ds_read_b128 v[184:187], v221 offset:53248
	ds_read_b128 v[188:191], v221 offset:54272
	ds_read_b128 v[202:205], v221 offset:55296
	ds_read_b128 v[206:209], v221 offset:56320
	s_add_u32 s70, s46, s78
	s_addc_u32 s71, s47, s79
	global_load_lds_dwordx4 v194, s[70:71]
	s_mov_b32 m0, s40
	s_add_u32 s70, s46, s84
	s_addc_u32 s71, s47, s85
	global_load_lds_dwordx4 v194, s[70:71]
	s_mov_b32 m0, s41
	s_add_u32 s70, s46, s50
	s_addc_u32 s71, s47, s51
	global_load_lds_dwordx4 v194, s[70:71]
	s_mov_b32 m0, s42
	s_add_u32 s70, s46, s54
	s_addc_u32 s71, s47, s55
	global_load_lds_dwordx4 v194, s[70:71]
	s_mov_b32 m0, s27
	s_add_u32 s70, s44, s78
	s_addc_u32 s71, s45, s79
	global_load_lds_dwordx4 v196, s[70:71]
	s_mov_b32 m0, s28
	s_add_u32 s70, s44, s92
	s_addc_u32 s71, s45, s93
	global_load_lds_dwordx4 v196, s[70:71]
	s_waitcnt vmcnt(8) lgkmcnt(0)
	s_barrier
	v_mfma_f32_16x16x32_bf16 v[64:67], v[136:139], v[168:171], v[64:67]
	v_mfma_f32_16x16x32_bf16 v[64:67], v[140:143], v[172:175], v[64:67]
	v_mfma_f32_16x16x32_bf16 v[60:63], v[144:147], v[168:171], v[60:63]
	v_mfma_f32_16x16x32_bf16 v[60:63], v[148:151], v[172:175], v[60:63]
	v_mfma_f32_16x16x32_bf16 v[56:59], v[152:155], v[168:171], v[56:59]
	v_mfma_f32_16x16x32_bf16 v[56:59], v[156:159], v[172:175], v[56:59]
	v_mfma_f32_16x16x32_bf16 v[52:55], v[160:163], v[168:171], v[52:55]
	v_mfma_f32_16x16x32_bf16 v[52:55], v[164:167], v[172:175], v[52:55]
	v_mfma_f32_16x16x32_bf16 v[36:39], v[160:163], v[176:179], v[36:39]
	v_mfma_f32_16x16x32_bf16 v[36:39], v[164:167], v[180:183], v[36:39]
	v_mfma_f32_16x16x32_bf16 v[40:43], v[152:155], v[176:179], v[40:43]
	v_mfma_f32_16x16x32_bf16 v[40:43], v[156:159], v[180:183], v[40:43]
	v_mfma_f32_16x16x32_bf16 v[44:47], v[144:147], v[176:179], v[44:47]
	v_mfma_f32_16x16x32_bf16 v[44:47], v[148:151], v[180:183], v[44:47]
	v_mfma_f32_16x16x32_bf16 v[48:51], v[136:139], v[176:179], v[48:51]
	v_mfma_f32_16x16x32_bf16 v[48:51], v[140:143], v[180:183], v[48:51]
	v_mfma_f32_16x16x32_bf16 v[32:35], v[136:139], v[184:187], v[32:35]
	v_mfma_f32_16x16x32_bf16 v[32:35], v[140:143], v[188:191], v[32:35]
	v_mfma_f32_16x16x32_bf16 v[28:31], v[144:147], v[184:187], v[28:31]
	v_mfma_f32_16x16x32_bf16 v[28:31], v[148:151], v[188:191], v[28:31]
	v_mfma_f32_16x16x32_bf16 v[24:27], v[152:155], v[184:187], v[24:27]
	v_mfma_f32_16x16x32_bf16 v[24:27], v[156:159], v[188:191], v[24:27]
	v_mfma_f32_16x16x32_bf16 v[20:23], v[160:163], v[184:187], v[20:23]
	v_mfma_f32_16x16x32_bf16 v[20:23], v[164:167], v[188:191], v[20:23]
	v_mfma_f32_16x16x32_bf16 v[4:7], v[160:163], v[202:205], v[4:7]
	v_mfma_f32_16x16x32_bf16 v[4:7], v[164:167], v[206:209], v[4:7]
	v_mfma_f32_16x16x32_bf16 v[8:11], v[152:155], v[202:205], v[8:11]
	v_mfma_f32_16x16x32_bf16 v[8:11], v[156:159], v[206:209], v[8:11]
	v_mfma_f32_16x16x32_bf16 v[12:15], v[144:147], v[202:205], v[12:15]
	v_mfma_f32_16x16x32_bf16 v[12:15], v[148:151], v[206:209], v[12:15]
	v_mfma_f32_16x16x32_bf16 v[16:19], v[136:139], v[202:205], v[16:19]
	v_mfma_f32_16x16x32_bf16 v[16:19], v[140:143], v[206:209], v[16:19]
	s_barrier
	s_add_i32 s15, s15, 2
	s_add_u32 s20, s20, 0x100
	s_addc_u32 s21, s21, 0
	s_add_u32 s8, s8, 0x100
	s_addc_u32 s9, s9, 0
	s_cmp_gt_u32 s15, 29
	s_cbranch_scc0 .LBB0_594
	s_and_b64 vcc, exec, s[12:13]
	s_cbranch_vccz .LBB0_597
	s_barrier

.LBB0_700:
	ds_read_b128 v[120:123], v116
	ds_read_b128 v[132:135], v116 offset:1024
	ds_read_b128 v[144:147], v116 offset:2048
	ds_read_b128 v[148:151], v116 offset:3072
	ds_read_b128 v[152:155], v117
	ds_read_b128 v[156:159], v117 offset:1024
	ds_read_b128 v[166:169], v117 offset:2048
	ds_read_b128 v[170:173], v117 offset:3072
	s_add_u32 s27, s10, 0xfff7c080
	s_addc_u32 s47, s11, -1
	s_cmp_eq_u32 s26, 28
	s_cselect_b32 s49, s21, s47
	s_cselect_b32 s48, s20, s27
	s_cselect_b32 s51, s3, s25
	s_cselect_b32 s50, s4, s24
	s_mov_b32 m0, s5
	ds_read_b128 v[180:183], v178
	ds_read_b128 v[184:187], v178 offset:1024
	ds_read_b128 v[188:191], v178 offset:2048
	ds_read_b128 v[192:195], v178 offset:3072
	ds_read_b128 v[196:199], v178 offset:4096
	ds_read_b128 v[200:203], v178 offset:5120
	ds_read_b128 v[204:207], v178 offset:6144
	ds_read_b128 v[214:217], v178 offset:7168
	global_load_lds_dwordx4 v164, s[10:11]
	s_mov_b32 m0, s19
	s_add_u32 s70, s10, s96
	s_addc_u32 s71, s11, s97
	global_load_lds_dwordx4 v164, s[70:71]
	s_waitcnt vmcnt(8) lgkmcnt(0)
	s_barrier
	v_mfma_f32_16x16x32_bf16 v[140:143], v[120:123], v[180:183], v[140:143]
	v_mfma_f32_16x16x32_bf16 v[140:143], v[132:135], v[184:187], v[140:143]
	v_mfma_f32_16x16x32_bf16 v[136:139], v[144:147], v[180:183], v[136:139]
	v_mfma_f32_16x16x32_bf16 v[136:139], v[148:151], v[184:187], v[136:139]
	v_mfma_f32_16x16x32_bf16 v[128:131], v[152:155], v[180:183], v[128:131]
	v_mfma_f32_16x16x32_bf16 v[128:131], v[156:159], v[184:187], v[128:131]
	v_mfma_f32_16x16x32_bf16 v[124:127], v[166:169], v[180:183], v[124:127]
	v_mfma_f32_16x16x32_bf16 v[124:127], v[170:173], v[184:187], v[124:127]
	v_mfma_f32_16x16x32_bf16 v[100:103], v[166:169], v[188:191], v[100:103]
	v_mfma_f32_16x16x32_bf16 v[100:103], v[170:173], v[192:195], v[100:103]
	v_mfma_f32_16x16x32_bf16 v[104:107], v[152:155], v[188:191], v[104:107]
	v_mfma_f32_16x16x32_bf16 v[104:107], v[156:159], v[192:195], v[104:107]
	v_mfma_f32_16x16x32_bf16 v[108:111], v[144:147], v[188:191], v[108:111]
	v_mfma_f32_16x16x32_bf16 v[108:111], v[148:151], v[192:195], v[108:111]
	v_mfma_f32_16x16x32_bf16 v[112:115], v[120:123], v[188:191], v[112:115]
	v_mfma_f32_16x16x32_bf16 v[112:115], v[132:135], v[192:195], v[112:115]
	v_mfma_f32_16x16x32_bf16 v[96:99], v[120:123], v[196:199], v[96:99]
	v_mfma_f32_16x16x32_bf16 v[96:99], v[132:135], v[200:203], v[96:99]
	v_mfma_f32_16x16x32_bf16 v[92:95], v[144:147], v[196:199], v[92:95]
	v_mfma_f32_16x16x32_bf16 v[92:95], v[148:151], v[200:203], v[92:95]
	v_mfma_f32_16x16x32_bf16 v[88:91], v[152:155], v[196:199], v[88:91]
	v_mfma_f32_16x16x32_bf16 v[88:91], v[156:159], v[200:203], v[88:91]
	v_mfma_f32_16x16x32_bf16 v[84:87], v[166:169], v[196:199], v[84:87]
	v_mfma_f32_16x16x32_bf16 v[84:87], v[170:173], v[200:203], v[84:87]
	v_mfma_f32_16x16x32_bf16 v[68:71], v[166:169], v[204:207], v[68:71]
	v_mfma_f32_16x16x32_bf16 v[68:71], v[170:173], v[214:217], v[68:71]
	v_mfma_f32_16x16x32_bf16 v[72:75], v[152:155], v[204:207], v[72:75]
	v_mfma_f32_16x16x32_bf16 v[72:75], v[156:159], v[214:217], v[72:75]
	v_mfma_f32_16x16x32_bf16 v[76:79], v[144:147], v[204:207], v[76:79]
	v_mfma_f32_16x16x32_bf16 v[76:79], v[148:151], v[214:217], v[76:79]
	v_mfma_f32_16x16x32_bf16 v[80:83], v[120:123], v[204:207], v[80:83]
	v_mfma_f32_16x16x32_bf16 v[80:83], v[132:135], v[214:217], v[80:83]
	s_barrier
	s_mov_b32 m0, s33
	ds_read_b128 v[180:183], v178 offset:16384
	ds_read_b128 v[184:187], v178 offset:17408
	ds_read_b128 v[188:191], v178 offset:18432
	ds_read_b128 v[192:195], v178 offset:19456
	ds_read_b128 v[196:199], v178 offset:20480
	ds_read_b128 v[200:203], v178 offset:21504
	ds_read_b128 v[204:207], v178 offset:22528
	ds_read_b128 v[214:217], v178 offset:23552
	global_load_lds_dwordx4 v160, s[50:51]
	s_mov_b32 m0, s40
	s_add_u32 s70, s50, s90
	s_addc_u32 s71, s51, s91
	global_load_lds_dwordx4 v160, s[70:71]
	s_mov_b32 m0, s41
	s_add_u32 s70, s50, s52
	s_addc_u32 s71, s51, s53
	global_load_lds_dwordx4 v160, s[70:71]
	s_mov_b32 m0, s42
	s_add_u32 s70, s50, s56
	s_addc_u32 s71, s51, s57
	global_load_lds_dwordx4 v160, s[70:71]
	s_mov_b32 m0, s29
	s_nop 0
	global_load_lds_dwordx4 v162, s[48:49]
	s_mov_b32 m0, s30
	s_add_u32 s70, s48, s96
	s_addc_u32 s71, s49, s97
	global_load_lds_dwordx4 v162, s[70:71]
	s_waitcnt vmcnt(8) lgkmcnt(0)
	s_barrier
	v_mfma_f32_16x16x32_bf16 v[56:59], v[120:123], v[180:183], v[56:59]
	v_mfma_f32_16x16x32_bf16 v[56:59], v[132:135], v[184:187], v[56:59]
	v_mfma_f32_16x16x32_bf16 v[52:55], v[144:147], v[180:183], v[52:55]
	v_mfma_f32_16x16x32_bf16 v[52:55], v[148:151], v[184:187], v[52:55]
	v_mfma_f32_16x16x32_bf16 v[64:67], v[152:155], v[180:183], v[64:67]
	v_mfma_f32_16x16x32_bf16 v[64:67], v[156:159], v[184:187], v[64:67]
	v_mfma_f32_16x16x32_bf16 v[60:63], v[166:169], v[180:183], v[60:63]
	v_mfma_f32_16x16x32_bf16 v[60:63], v[170:173], v[184:187], v[60:63]
	v_mfma_f32_16x16x32_bf16 v[36:39], v[166:169], v[188:191], v[36:39]
	v_mfma_f32_16x16x32_bf16 v[36:39], v[170:173], v[192:195], v[36:39]
	v_mfma_f32_16x16x32_bf16 v[40:43], v[152:155], v[188:191], v[40:43]
	v_mfma_f32_16x16x32_bf16 v[40:43], v[156:159], v[192:195], v[40:43]
	v_mfma_f32_16x16x32_bf16 v[44:47], v[144:147], v[188:191], v[44:47]
	v_mfma_f32_16x16x32_bf16 v[44:47], v[148:151], v[192:195], v[44:47]
	v_mfma_f32_16x16x32_bf16 v[48:51], v[120:123], v[188:191], v[48:51]
	v_mfma_f32_16x16x32_bf16 v[48:51], v[132:135], v[192:195], v[48:51]
	v_mfma_f32_16x16x32_bf16 v[32:35], v[120:123], v[196:199], v[32:35]
	v_mfma_f32_16x16x32_bf16 v[32:35], v[132:135], v[200:203], v[32:35]
	v_mfma_f32_16x16x32_bf16 v[28:31], v[144:147], v[196:199], v[28:31]
	v_mfma_f32_16x16x32_bf16 v[28:31], v[148:151], v[200:203], v[28:31]
	v_mfma_f32_16x16x32_bf16 v[24:27], v[152:155], v[196:199], v[24:27]
	v_mfma_f32_16x16x32_bf16 v[24:27], v[156:159], v[200:203], v[24:27]
	v_mfma_f32_16x16x32_bf16 v[20:23], v[166:169], v[196:199], v[20:23]
	v_mfma_f32_16x16x32_bf16 v[20:23], v[170:173], v[200:203], v[20:23]
	v_mfma_f32_16x16x32_bf16 v[4:7], v[166:169], v[204:207], v[4:7]
	v_mfma_f32_16x16x32_bf16 v[4:7], v[170:173], v[214:217], v[4:7]
	v_mfma_f32_16x16x32_bf16 v[8:11], v[152:155], v[204:207], v[8:11]
	v_mfma_f32_16x16x32_bf16 v[8:11], v[156:159], v[214:217], v[8:11]
	v_mfma_f32_16x16x32_bf16 v[12:15], v[144:147], v[204:207], v[12:15]
	v_mfma_f32_16x16x32_bf16 v[12:15], v[148:151], v[214:217], v[12:15]
	v_mfma_f32_16x16x32_bf16 v[16:19], v[120:123], v[204:207], v[16:19]
	v_mfma_f32_16x16x32_bf16 v[16:19], v[132:135], v[214:217], v[16:19]
	s_barrier
; #define PG8_MMA(ai, bj, At, Bt) do { __builtin_amdgcn_s_setprio(1); _Pragma("unroll") for (int m = 0; m < 4; ++m) _Pragma("unroll") for (int n = 0; n < 2; ++n) _Pragma("unroll") for (int k = 0; k < 2; ++k) \
;         acc[ai][bj][m][n] = __builtin_amdgcn_mfma_f32_16x16x32_bf16(Bt[n][k], At[m][k], acc[ai][bj][m][n], 0, 0, 0); __builtin_amdgcn_s_setprio(0); } while (0)
; #define PG8_WAIT_V(n) asm volatile("s_waitcnt vmcnt(" #n ")" ::: "memory")
; #define PG8_TRIP_HEAD(T) const int t = (T); const bool last = (t == nt - 2); \
;             const char* a1 = cA + (size_t)(t + 1) * kstep; \
;             const char* a2 = last ? nA : cA + (size_t)(t + 2) * kstep; const char* b2 = last ? nB : cB + (size_t)(t + 2) * kstep; \
;             const char* a3 = a2 + kstep; const char* b3 = b2 + kstep; \
;             if (last && has_next) S.a_ready(nxt);
; template <class Epi, class Sched, bool ALIGN_EPI = false, bool SP2 = false>
; __device__ __forceinline__ void gemm_phase(PG8_LAS unsigned char* lds, const Gemm g, const Sched& S, const Epi& E) {
;     ...
;         if constexpr (SP2) {
;             { PG8_TRIP_HEAD(0) PG8_TRIP_SP2(asm volatile("s_waitcnt vmcnt(%0)" :: "n"(8 + Epi::NST) : "memory"), PG8_MMAZ) }
;             for (int tt = 2; tt < nt; tt += 2) { PG8_TRIP_HEAD(tt) PG8_TRIP_SP2(PG8_WAIT_V(8), PG8_MMA) }
	ds_read_b128 v[120:123], v118
	ds_read_b128 v[132:135], v118 offset:1024
	ds_read_b128 v[144:147], v118 offset:2048
	ds_read_b128 v[148:151], v118 offset:3072
	ds_read_b128 v[152:155], v119
	ds_read_b128 v[156:159], v119 offset:1024
	ds_read_b128 v[166:169], v119 offset:2048
	ds_read_b128 v[170:173], v119 offset:3072
	s_mov_b32 m0, s31
	ds_read_b128 v[180:183], v178 offset:32768
	ds_read_b128 v[184:187], v178 offset:33792
	ds_read_b128 v[188:191], v178 offset:34816
	ds_read_b128 v[192:195], v178 offset:35840
	ds_read_b128 v[196:199], v178 offset:36864
	ds_read_b128 v[200:203], v178 offset:37888
	ds_read_b128 v[204:207], v178 offset:38912
	ds_read_b128 v[214:217], v178 offset:39936
	s_add_u32 s70, s48, s82
	s_addc_u32 s71, s49, s83
	global_load_lds_dwordx4 v162, s[70:71]
	s_mov_b32 m0, s34
	s_add_u32 s70, s48, s62
	s_addc_u32 s71, s49, s63
	global_load_lds_dwordx4 v162, s[70:71]
	s_waitcnt vmcnt(8) lgkmcnt(0)
	s_barrier
	v_mfma_f32_16x16x32_bf16 v[140:143], v[120:123], v[180:183], v[140:143]
	v_mfma_f32_16x16x32_bf16 v[140:143], v[132:135], v[184:187], v[140:143]
	v_mfma_f32_16x16x32_bf16 v[136:139], v[144:147], v[180:183], v[136:139]
	v_mfma_f32_16x16x32_bf16 v[136:139], v[148:151], v[184:187], v[136:139]
	v_mfma_f32_16x16x32_bf16 v[128:131], v[152:155], v[180:183], v[128:131]
	v_mfma_f32_16x16x32_bf16 v[128:131], v[156:159], v[184:187], v[128:131]
	v_mfma_f32_16x16x32_bf16 v[124:127], v[166:169], v[180:183], v[124:127]
	v_mfma_f32_16x16x32_bf16 v[124:127], v[170:173], v[184:187], v[124:127]
	v_mfma_f32_16x16x32_bf16 v[100:103], v[166:169], v[188:191], v[100:103]
	v_mfma_f32_16x16x32_bf16 v[100:103], v[170:173], v[192:195], v[100:103]
	v_mfma_f32_16x16x32_bf16 v[104:107], v[152:155], v[188:191], v[104:107]
	v_mfma_f32_16x16x32_bf16 v[104:107], v[156:159], v[192:195], v[104:107]
	v_mfma_f32_16x16x32_bf16 v[108:111], v[144:147], v[188:191], v[108:111]
	v_mfma_f32_16x16x32_bf16 v[108:111], v[148:151], v[192:195], v[108:111]
	v_mfma_f32_16x16x32_bf16 v[112:115], v[120:123], v[188:191], v[112:115]
	v_mfma_f32_16x16x32_bf16 v[112:115], v[132:135], v[192:195], v[112:115]
	v_mfma_f32_16x16x32_bf16 v[96:99], v[120:123], v[196:199], v[96:99]
	v_mfma_f32_16x16x32_bf16 v[96:99], v[132:135], v[200:203], v[96:99]
	v_mfma_f32_16x16x32_bf16 v[92:95], v[144:147], v[196:199], v[92:95]
	v_mfma_f32_16x16x32_bf16 v[92:95], v[148:151], v[200:203], v[92:95]
	v_mfma_f32_16x16x32_bf16 v[88:91], v[152:155], v[196:199], v[88:91]
	v_mfma_f32_16x16x32_bf16 v[88:91], v[156:159], v[200:203], v[88:91]
	v_mfma_f32_16x16x32_bf16 v[84:87], v[166:169], v[196:199], v[84:87]
	v_mfma_f32_16x16x32_bf16 v[84:87], v[170:173], v[200:203], v[84:87]
	v_mfma_f32_16x16x32_bf16 v[68:71], v[166:169], v[204:207], v[68:71]
	v_mfma_f32_16x16x32_bf16 v[68:71], v[170:173], v[214:217], v[68:71]
	v_mfma_f32_16x16x32_bf16 v[72:75], v[152:155], v[204:207], v[72:75]
	v_mfma_f32_16x16x32_bf16 v[72:75], v[156:159], v[214:217], v[72:75]
	v_mfma_f32_16x16x32_bf16 v[76:79], v[144:147], v[204:207], v[76:79]
	v_mfma_f32_16x16x32_bf16 v[76:79], v[148:151], v[214:217], v[76:79]
	v_mfma_f32_16x16x32_bf16 v[80:83], v[120:123], v[204:207], v[80:83]
	v_mfma_f32_16x16x32_bf16 v[80:83], v[132:135], v[214:217], v[80:83]
	s_barrier
	s_mov_b32 m0, s43
	ds_read_b128 v[180:183], v178 offset:49152
	ds_read_b128 v[184:187], v178 offset:50176
	ds_read_b128 v[188:191], v178 offset:51200
	ds_read_b128 v[192:195], v178 offset:52224
	ds_read_b128 v[196:199], v178 offset:53248
	ds_read_b128 v[200:203], v178 offset:54272
	ds_read_b128 v[204:207], v178 offset:55296
	ds_read_b128 v[214:217], v178 offset:56320
	s_add_u32 s70, s50, s78
	s_addc_u32 s71, s51, s79
	global_load_lds_dwordx4 v160, s[70:71]
	s_mov_b32 m0, s44
	s_add_u32 s70, s50, s84
	s_addc_u32 s71, s51, s85
	global_load_lds_dwordx4 v160, s[70:71]
	s_mov_b32 m0, s45
	s_add_u32 s70, s50, s54
	s_addc_u32 s71, s51, s55
	global_load_lds_dwordx4 v160, s[70:71]
	s_mov_b32 m0, s46
	s_add_u32 s70, s50, s60
	s_addc_u32 s71, s51, s61
	global_load_lds_dwordx4 v160, s[70:71]
	s_mov_b32 m0, s36
	s_add_u32 s70, s48, s78
	s_addc_u32 s71, s49, s79
	global_load_lds_dwordx4 v162, s[70:71]
	s_mov_b32 m0, s37
	s_add_u32 s70, s48, s92
	s_addc_u32 s71, s49, s93
	global_load_lds_dwordx4 v162, s[70:71]
	s_waitcnt vmcnt(8) lgkmcnt(0)
	s_barrier
	v_mfma_f32_16x16x32_bf16 v[56:59], v[120:123], v[180:183], v[56:59]
	v_mfma_f32_16x16x32_bf16 v[56:59], v[132:135], v[184:187], v[56:59]
	v_mfma_f32_16x16x32_bf16 v[52:55], v[144:147], v[180:183], v[52:55]
	v_mfma_f32_16x16x32_bf16 v[52:55], v[148:151], v[184:187], v[52:55]
	v_mfma_f32_16x16x32_bf16 v[64:67], v[152:155], v[180:183], v[64:67]
	v_mfma_f32_16x16x32_bf16 v[64:67], v[156:159], v[184:187], v[64:67]
	v_mfma_f32_16x16x32_bf16 v[60:63], v[166:169], v[180:183], v[60:63]
	v_mfma_f32_16x16x32_bf16 v[60:63], v[170:173], v[184:187], v[60:63]
	v_mfma_f32_16x16x32_bf16 v[36:39], v[166:169], v[188:191], v[36:39]
	v_mfma_f32_16x16x32_bf16 v[36:39], v[170:173], v[192:195], v[36:39]
	v_mfma_f32_16x16x32_bf16 v[40:43], v[152:155], v[188:191], v[40:43]
	v_mfma_f32_16x16x32_bf16 v[40:43], v[156:159], v[192:195], v[40:43]
	v_mfma_f32_16x16x32_bf16 v[44:47], v[144:147], v[188:191], v[44:47]
	v_mfma_f32_16x16x32_bf16 v[44:47], v[148:151], v[192:195], v[44:47]
	v_mfma_f32_16x16x32_bf16 v[48:51], v[120:123], v[188:191], v[48:51]
	v_mfma_f32_16x16x32_bf16 v[48:51], v[132:135], v[192:195], v[48:51]
	v_mfma_f32_16x16x32_bf16 v[32:35], v[120:123], v[196:199], v[32:35]
	v_mfma_f32_16x16x32_bf16 v[32:35], v[132:135], v[200:203], v[32:35]
	v_mfma_f32_16x16x32_bf16 v[28:31], v[144:147], v[196:199], v[28:31]
	v_mfma_f32_16x16x32_bf16 v[28:31], v[148:151], v[200:203], v[28:31]
	v_mfma_f32_16x16x32_bf16 v[24:27], v[152:155], v[196:199], v[24:27]
	v_mfma_f32_16x16x32_bf16 v[24:27], v[156:159], v[200:203], v[24:27]
	v_mfma_f32_16x16x32_bf16 v[20:23], v[166:169], v[196:199], v[20:23]
	v_mfma_f32_16x16x32_bf16 v[20:23], v[170:173], v[200:203], v[20:23]
	v_mfma_f32_16x16x32_bf16 v[4:7], v[166:169], v[204:207], v[4:7]
	v_mfma_f32_16x16x32_bf16 v[4:7], v[170:173], v[214:217], v[4:7]
	v_mfma_f32_16x16x32_bf16 v[8:11], v[152:155], v[204:207], v[8:11]
	v_mfma_f32_16x16x32_bf16 v[8:11], v[156:159], v[214:217], v[8:11]
	v_mfma_f32_16x16x32_bf16 v[12:15], v[144:147], v[204:207], v[12:15]
	v_mfma_f32_16x16x32_bf16 v[12:15], v[148:151], v[214:217], v[12:15]
	v_mfma_f32_16x16x32_bf16 v[16:19], v[120:123], v[204:207], v[16:19]
	v_mfma_f32_16x16x32_bf16 v[16:19], v[132:135], v[214:217], v[16:19]
	s_barrier
	s_add_i32 s26, s26, 2
	s_add_u32 s10, s10, 0x100
	s_addc_u32 s11, s11, 0
	s_add_u32 s24, s24, 0x100
	s_addc_u32 s25, s25, 0
	s_cmp_gt_u32 s26, 29
	s_cbranch_scc0 .LBB0_700
	s_and_b64 vcc, exec, s[16:17]
	s_cbranch_vccz .LBB0_703
	s_barrier
